# MoE gate/up GEMM phases: bias quads prefetched at the unit header (epilogue no longer drains the vector-memory queue), next-unit gathered row offsets fetched as one batch behind one wait
# speedup vs baseline: 1.0148x; 1.0009x over previous
;     __device__ __forceinline__ bool next(int i, Unit& u) const {
;         const int L = i * G + vcu;
;         if (L >= tab[96]) return false;
;         const int me = threadIdx.x & 31;
;         const int st_l = tab[me], c_l = tab[32 + me];
;         const unsigned long long m = __ballot(L >= st_l && L < st_l + ((c_l + 255) >> 8) * nN);
;         const int e = __builtin_amdgcn_readfirstlane(__builtin_ctzll(m) & 31);
;         const int st = tab[e], c = tab[32 + e], ab = tab[64 + e];
;         const int l = L - st;
;         const int sh = nN == 8 ? 3 : 2;
;         u.e = e; u.pm = l >> sh; u.pn = l & (nN - 1); u.aux = ab; u.cnt = c;
;         u.a = gather ? Abase : Abase + (size_t)(ab + u.pm * 256) * 1024 * 2; u.b = Bbase + (size_t)e * bstride + (size_t)u.pn * 256 * K * 2; return true;
;     __device__ __forceinline__ void operator()(const f32x4 (&acc)[2][2][4][2], const Unit& u, int wr, int wc, int fr, int fq) const {
;     ...
;         const float* bgu = P.in[35] + (size_t)(layer * NE + u.e) * 2048;
;         const int cl = u.pn * 128 + wc * 32 + 8 * fq;
;         f32x4 bg[2], bu[2];
; #pragma unroll
;         for (int n = 0; n < 2; ++n) { bg[n] = *(const f32x4*)(bgu + cl + 4 * n); bu[n] = *(const f32x4*)(bgu + 1024 + cl + 4 * n) + 1.f; }
.LBB0_1495:
	s_lshl_b32 s32, s20, 13
	v_mov_b32_e32 v16, s32
	v_mov_b32_e32 v17, 0
	v_lshl_add_u64 v[16:17], v[16:17], 0, s[70:71]
	v_lshl_or_b32 v18, s51, 7, v154
	v_ashrrev_i32_e32 v19, 31, v18
	v_lshl_add_u64 v[20:21], v[18:19], 2, v[16:17]
	v_mov_b32_e32 v22, s42
	v_mov_b32_e32 v23, 0
	v_lshl_add_u64 v[22:23], v[22:23], 0, v[20:21]
	v_mov_b32_e32 v24, 0x1000
	v_mov_b32_e32 v25, 0
	v_lshl_add_u64 v[24:25], v[24:25], 0, v[20:21]
	global_load_dwordx4 v[240:243], v[20:21], off
	global_load_dwordx4 v[244:247], v[20:21], off offset:16
	global_load_dwordx4 v[248:251], v[22:23], off
	global_load_dwordx4 v[182:185], v[24:25], off offset:16
	ds_read_b32 v2, v155
	s_add_i32 s39, s39, 1
	s_mul_i32 s21, s39, s62
	v_readlane_b32 s0, v254, 2
	s_add_i32 s21, s21, s0
	s_waitcnt lgkmcnt(0)
	v_cmp_ge_i32_e32 vcc, s21, v2
	v_cmp_lt_i32_e64 s[0:1], s21, v2
	s_cbranch_vccnz .LBB0_1499
	ds_read_b32 v2, v148
	s_mov_b64 s[18:19], 0
	s_waitcnt lgkmcnt(0)
	v_cmp_ge_i32_e32 vcc, s21, v2
	s_and_saveexec_b64 s[4:5], vcc
	s_cbranch_execz .LBB0_1498
	ds_read_b32 v3, v148 offset:128
	s_waitcnt lgkmcnt(0)
	v_add_u32_e32 v3, 0xff, v3
	v_ashrrev_i32_e32 v3, 5, v3
	v_and_b32_e32 v3, -8, v3
	v_add_u32_e32 v2, v3, v2
	v_cmp_lt_i32_e32 vcc, s21, v2
	s_and_b64 s[18:19], vcc, exec

; template <class Epi, class Sched, bool GATHER, bool ALIGN_EPI, bool PFB = false>
; __device__ __forceinline__ void gemm_phase(LAS unsigned char* lds, const int lda, const int K, const Sched& S, const Epi& E) {
;     ...
;         if (GATHER) {
; #pragma unroll
;             for (int i = 0; i < 2; ++i) { if (has_next) { nA0[i] = S.arow_off(nxt, Rr[i]) + (unsigned)Cc[i] * 2u; nA1[i] = S.arow_off(nxt, HALF + Rr[i]) + (unsigned)Cc[i] * 2u; } else { nA0[i] = vA0[i]; nA1[i] = vA1[i]; } }
;         }
;     __device__ __forceinline__ unsigned arow_off(const Unit& u, int r) const { int rr = u.pm * 256 + r; rr = rr < u.cnt ? rr : u.cnt - 1; return (unsigned)rowtab[(size_t)u.e * R + rr] * (unsigned)(D * 2); }
.LBB0_1499:
	s_lshl_b32 s21, s49, 8
	s_mul_i32 s5, s47, 0x11000
	s_mul_hi_i32 s4, s47, 0x11000
	s_add_u32 s24, s29, s5
	v_cndmask_b32_e64 v3, 0, 1, s[0:1]
	v_add_u32_e32 v2, -1, v145
	s_addc_u32 s25, s30, s4
	s_or_b32 s26, s21, 0x80
	v_cmp_ne_u32_e64 s[4:5], 1, v3
	s_andn2_b64 vcc, exec, s[0:1]
	v_mov_b32_e32 v144, v99
	v_mov_b32_e32 v161, v100
	s_cbranch_vccnz .LBB0_1501
	v_or_b32_e32 v3, s21, v149
	v_min_i32_e32 v4, v3, v2
	v_or_b32_e32 v3, s26, v149
	v_ashrrev_i32_e32 v5, 31, v4
	v_min_i32_e32 v6, v3, v2
	v_lshl_add_u64 v[4:5], v[4:5], 2, s[24:25]
	v_ashrrev_i32_e32 v7, 31, v6
	v_lshl_add_u64 v[6:7], v[6:7], 2, s[24:25]
	v_or_b32_e32 v8, s21, v150
	v_min_i32_e32 v8, v8, v2
	v_add_u32_e32 v10, s26, v150
	v_min_i32_e32 v10, v10, v2
	v_ashrrev_i32_e32 v9, 31, v8
	v_ashrrev_i32_e32 v11, 31, v10
	v_lshl_add_u64 v[8:9], v[8:9], 2, s[24:25]
	v_lshl_add_u64 v[10:11], v[10:11], 2, s[24:25]
	global_load_dword v12, v[4:5], off
	global_load_dword v13, v[6:7], off
	global_load_dword v14, v[8:9], off
	global_load_dword v15, v[10:11], off
	s_waitcnt vmcnt(0)
	v_lshl_or_b32 v144, v12, 11, v151
	v_lshl_or_b32 v161, v13, 11, v151
.LBB0_1501:
	s_and_b64 vcc, exec, s[4:5]
	v_mov_b32_e32 v162, v98
	v_mov_b32_e32 v163, v106
	s_cbranch_vccnz .LBB0_1503
	v_lshl_or_b32 v162, v14, 11, v151
	v_lshl_or_b32 v163, v15, 11, v151

; __device__ __forceinline__ unsigned cvt_pk_bf16(float lo, float hi) { unsigned r; asm volatile("v_cvt_pk_bf16_f32 %0, %1, %2" : "=v"(r) : "v"(lo), "v"(hi)); return r; }
;     __device__ __forceinline__ void operator()(const f32x4 (&acc)[2][2][4][2], const Unit& u, int wr, int wc, int fr, int fq) const {
;     ...
;         const float* bgu = P.in[35] + (size_t)(layer * NE + u.e) * 2048;
;         const int cl = u.pn * 128 + wc * 32 + 8 * fq;
;         f32x4 bg[2], bu[2];
; #pragma unroll
;         for (int n = 0; n < 2; ++n) { bg[n] = *(const f32x4*)(bgu + cl + 4 * n); bu[n] = *(const f32x4*)(bgu + 1024 + cl + 4 * n) + 1.f; }
;         bf16* act = (bf16*)(P.ws + WS_ACT) + (size_t)(u.aux + u.pm * 256 + wr * 64 + fr) * 1024 + cl;
;         const f32x2 kk = {-1.702f * LOG2E, -1.702f * LOG2E}, one2 = {1.f, 1.f};
; #pragma unroll
;         for (int ai = 0; ai < 2; ++ai)
; #pragma unroll
;             for (int m = 0; m < 4; ++m) { unsigned wv[4];
; #pragma unroll
;                 for (int n = 0; n < 2; ++n)
; #pragma unroll
;                     for (int jp = 0; jp < 2; ++jp) {
;                         f32x2 g = (f32x2){acc[ai][0][m][n][2 * jp], acc[ai][0][m][n][2 * jp + 1]} + (f32x2){bg[n][2 * jp], bg[n][2 * jp + 1]};
;                         f32x2 uu = (f32x2){acc[ai][1][m][n][2 * jp], acc[ai][1][m][n][2 * jp + 1]} + (f32x2){bu[n][2 * jp], bu[n][2 * jp + 1]};
;                         g.x = fminf(g.x, 7.f); g.y = fminf(g.y, 7.f);
;                         uu.x = __builtin_amdgcn_fmed3f(uu.x, -6.f, 8.f); uu.y = __builtin_amdgcn_fmed3f(uu.y, -6.f, 8.f);
;                         f32x2 t = g * kk;
;                         t.x = __builtin_amdgcn_exp2f(t.x); t.y = __builtin_amdgcn_exp2f(t.y);
;                         t = t + one2;
;                         t.x = __builtin_amdgcn_rcpf(t.x); t.y = __builtin_amdgcn_rcpf(t.y);
;                         const f32x2 o = uu * (g * t);
;                         wv[n * 2 + jp] = cvt_pk_bf16(o.x, o.y); }
;                 u32x4 w; w.x = wv[0]; w.y = wv[1]; w.z = wv[2]; w.w = wv[3];
;                 *(u32x4*)(act + (size_t)(ai * HALF + m * 16) * 1024) = w; }
.LBB0_1507:
	s_ashr_i32 s21, s20, 31
	s_lshl_b64 s[0:1], s[20:21], 13
	s_add_u32 s0, s70, s0
	v_lshl_or_b32 v146, s51, 7, v154
	s_addc_u32 s1, s71, s1
	v_ashrrev_i32_e32 v147, 31, v146
	v_lshl_add_u64 v[170:171], v[146:147], 2, s[0:1]
	v_add_co_u32_e32 v166, vcc, s42, v170
	s_mov_b64 s[0:1], 0x1000
	v_addc_co_u32_e32 v167, vcc, 0, v171, vcc
	v_lshl_add_u64 v[170:171], v[170:171], 0, s[0:1]
	s_lshl_b32 s0, s50, 8
	v_add_u32_e32 v142, s0, v164
	v_add_u32_e32 v164, v142, v152
	v_ashrrev_i32_e32 v165, 31, v164
	v_lshlrev_b64 v[164:165], 11, v[164:165]
	v_lshl_add_u64 v[164:165], s[12:13], 0, v[164:165]
	v_lshl_add_u64 v[146:147], v[146:147], 1, v[164:165]
	s_mov_b32 s0, 0x8000
	v_mov_b64_e32 v[106:107], v[240:241]
	v_mov_b64_e32 v[108:109], v[242:243]
	v_mov_b64_e32 v[98:99], v[244:245]
	v_mov_b64_e32 v[100:101], v[246:247]
	v_mov_b64_e32 v[166:167], v[248:249]
	v_mov_b64_e32 v[168:169], v[250:251]
	v_mov_b64_e32 v[170:171], v[182:183]
	v_mov_b64_e32 v[172:173], v[184:185]
	v_pk_add_f32 v[136:137], v[136:137], v[108:109]
	v_pk_add_f32 v[134:135], v[134:135], v[106:107]
	v_pk_add_f32 v[132:133], v[132:133], v[100:101]
	v_pk_add_f32 v[130:131], v[130:131], v[98:99]
	v_pk_add_f32 v[126:127], v[126:127], v[106:107]
	v_min_f32_e32 v134, 0x40e00000, v134
	v_min_f32_e32 v135, 0x40e00000, v135
	v_min_f32_e32 v136, 0x40e00000, v136
	v_min_f32_e32 v137, 0x40e00000, v137
	v_min_f32_e32 v174, 0x40e00000, v130
	v_min_f32_e32 v175, 0x40e00000, v131
	v_min_f32_e32 v176, 0x40e00000, v132
	v_min_f32_e32 v177, 0x40e00000, v133
	v_min_f32_e32 v178, 0x40e00000, v126
	v_min_f32_e32 v179, 0x40e00000, v127
	v_pk_add_f32 v[130:131], v[168:169], 1.0 op_sel_hi:[1,0]
	v_pk_add_f32 v[132:133], v[166:167], 1.0 op_sel_hi:[1,0]
	v_pk_mul_f32 v[166:167], v[134:135], s[16:17] op_sel_hi:[1,0]
	v_pk_mul_f32 v[168:169], v[136:137], s[16:17] op_sel_hi:[1,0]
	v_pk_add_f32 v[164:165], v[128:129], v[108:109]
	v_pk_add_f32 v[126:127], v[172:173], 1.0 op_sel_hi:[1,0]
	v_pk_add_f32 v[128:129], v[170:171], 1.0 op_sel_hi:[1,0]
	v_pk_mul_f32 v[170:171], v[174:175], s[16:17] op_sel_hi:[1,0]
	v_pk_mul_f32 v[172:173], v[176:177], s[16:17] op_sel_hi:[1,0]
	v_pk_mul_f32 v[180:181], v[178:179], s[16:17] op_sel_hi:[1,0]
	v_exp_f32_e32 v166, v166
	v_exp_f32_e32 v167, v167
	v_exp_f32_e32 v168, v168
	v_exp_f32_e32 v169, v169
	v_exp_f32_e32 v170, v170
	v_exp_f32_e32 v171, v171
	v_exp_f32_e32 v172, v172
	v_exp_f32_e32 v173, v173
	v_pk_add_f32 v[188:189], v[114:115], v[132:133]
	v_exp_f32_e32 v114, v180
	v_exp_f32_e32 v115, v181
	v_pk_add_f32 v[166:167], v[166:167], 1.0 op_sel_hi:[1,0]
	v_pk_add_f32 v[168:169], v[168:169], 1.0 op_sel_hi:[1,0]
	v_pk_add_f32 v[170:171], v[170:171], 1.0 op_sel_hi:[1,0]
	v_pk_add_f32 v[172:173], v[172:173], 1.0 op_sel_hi:[1,0]
	v_pk_add_f32 v[180:181], v[114:115], 1.0 op_sel_hi:[1,0]
	v_rcp_f32_e32 v114, v166
	v_rcp_f32_e32 v115, v167
	v_rcp_f32_e32 v166, v168
	v_rcp_f32_e32 v167, v169
	v_rcp_f32_e32 v168, v170
	v_rcp_f32_e32 v169, v171
	v_rcp_f32_e32 v170, v172
	v_rcp_f32_e32 v171, v173
	v_pk_add_f32 v[124:125], v[124:125], v[130:131]
	v_pk_add_f32 v[122:123], v[122:123], v[132:133]
	v_pk_add_f32 v[120:121], v[120:121], v[126:127]
	v_pk_add_f32 v[118:119], v[118:119], v[128:129]
	v_pk_add_f32 v[186:187], v[116:117], v[130:131]
	v_med3_f32 v116, v122, s43, v159
	v_med3_f32 v117, v123, s43, v159
	v_med3_f32 v122, v124, s43, v159
	v_med3_f32 v123, v125, s43, v159
	v_pk_mul_f32 v[114:115], v[134:135], v[114:115]
	v_pk_mul_f32 v[134:135], v[136:137], v[166:167]
	v_med3_f32 v118, v118, s43, v159
	v_med3_f32 v119, v119, s43, v159
	v_med3_f32 v120, v120, s43, v159
	v_med3_f32 v121, v121, s43, v159
	v_pk_mul_f32 v[136:137], v[174:175], v[168:169]
	v_pk_mul_f32 v[166:167], v[176:177], v[170:171]
	v_pk_mul_f32 v[114:115], v[116:117], v[114:115]
	v_pk_mul_f32 v[116:117], v[122:123], v[134:135]
	v_pk_mul_f32 v[118:119], v[118:119], v[136:137]
	v_pk_mul_f32 v[120:121], v[120:121], v[166:167]
	v_cvt_pk_bf16_f32 v114, v114, v115
	v_cvt_pk_bf16_f32 v115, v116, v117
	v_cvt_pk_bf16_f32 v116, v118, v119
	v_rcp_f32_e32 v172, v180
	v_cvt_pk_bf16_f32 v117, v120, v121
	global_store_dwordx4 v[146:147], v[114:117], off
	v_rcp_f32_e32 v173, v181
	v_med3_f32 v124, v188, s43, v159
	v_min_f32_e32 v116, 0x40e00000, v164
	v_min_f32_e32 v117, 0x40e00000, v165
	v_pk_mul_f32 v[114:115], v[116:117], s[16:17] op_sel_hi:[1,0]
	v_med3_f32 v125, v189, s43, v159
	v_exp_f32_e32 v114, v114
	v_exp_f32_e32 v115, v115
	v_pk_mul_f32 v[118:119], v[178:179], v[172:173]
	v_pk_add_f32 v[110:111], v[110:111], v[98:99]
	v_pk_mul_f32 v[118:119], v[124:125], v[118:119]
	v_pk_add_f32 v[114:115], v[114:115], 1.0 op_sel_hi:[1,0]
	v_min_f32_e32 v110, 0x40e00000, v110
	v_rcp_f32_e32 v120, v114
	v_rcp_f32_e32 v121, v115
	v_cvt_pk_bf16_f32 v114, v118, v119
	v_med3_f32 v118, v186, s43, v159
	v_med3_f32 v119, v187, s43, v159
	v_pk_mul_f32 v[116:117], v[116:117], v[120:121]
	v_min_f32_e32 v111, 0x40e00000, v111
	v_pk_mul_f32 v[116:117], v[118:119], v[116:117]
	v_pk_add_f32 v[112:113], v[112:113], v[100:101]
	v_cvt_pk_bf16_f32 v115, v116, v117
	v_pk_mul_f32 v[116:117], v[110:111], s[16:17] op_sel_hi:[1,0]
	v_min_f32_e32 v112, 0x40e00000, v112
	v_exp_f32_e32 v116, v116
	v_exp_f32_e32 v117, v117
	v_min_f32_e32 v113, 0x40e00000, v113
	v_pk_mul_f32 v[118:119], v[112:113], s[16:17] op_sel_hi:[1,0]
	v_pk_add_f32 v[102:103], v[102:103], v[128:129]
	v_pk_add_f32 v[116:117], v[116:117], 1.0 op_sel_hi:[1,0]
	v_exp_f32_e32 v118, v118
	v_rcp_f32_e32 v116, v116
	v_rcp_f32_e32 v117, v117
	v_exp_f32_e32 v119, v119
	v_med3_f32 v102, v102, s43, v159
	v_med3_f32 v103, v103, s43, v159
	v_pk_mul_f32 v[110:111], v[110:111], v[116:117]
; __device__ __forceinline__ unsigned cvt_pk_bf16(float lo, float hi) { unsigned r; asm volatile("v_cvt_pk_bf16_f32 %0, %1, %2" : "=v"(r) : "v"(lo), "v"(hi)); return r; }
;     __device__ __forceinline__ void operator()(const f32x4 (&acc)[2][2][4][2], const Unit& u, int wr, int wc, int fr, int fq) const {
;     ...
; #pragma unroll
;         for (int ai = 0; ai < 2; ++ai)
; #pragma unroll
;             for (int m = 0; m < 4; ++m) { unsigned wv[4];
; #pragma unroll
;                 for (int n = 0; n < 2; ++n)
; #pragma unroll
;                     for (int jp = 0; jp < 2; ++jp) {
;                         f32x2 g = (f32x2){acc[ai][0][m][n][2 * jp], acc[ai][0][m][n][2 * jp + 1]} + (f32x2){bg[n][2 * jp], bg[n][2 * jp + 1]};
;                         f32x2 uu = (f32x2){acc[ai][1][m][n][2 * jp], acc[ai][1][m][n][2 * jp + 1]} + (f32x2){bu[n][2 * jp], bu[n][2 * jp + 1]};
;                         g.x = fminf(g.x, 7.f); g.y = fminf(g.y, 7.f);
;                         uu.x = __builtin_amdgcn_fmed3f(uu.x, -6.f, 8.f); uu.y = __builtin_amdgcn_fmed3f(uu.y, -6.f, 8.f);
;                         f32x2 t = g * kk;
;                         t.x = __builtin_amdgcn_exp2f(t.x); t.y = __builtin_amdgcn_exp2f(t.y);
;                         t = t + one2;
;                         t.x = __builtin_amdgcn_rcpf(t.x); t.y = __builtin_amdgcn_rcpf(t.y);
;                         const f32x2 o = uu * (g * t);
;                         wv[n * 2 + jp] = cvt_pk_bf16(o.x, o.y); }
;                 u32x4 w; w.x = wv[0]; w.y = wv[1]; w.z = wv[2]; w.w = wv[3];
;                 *(u32x4*)(act + (size_t)(ai * HALF + m * 16) * 1024) = w; }
	v_pk_add_f32 v[104:105], v[104:105], v[126:127]
	v_pk_mul_f32 v[102:103], v[102:103], v[110:111]
	v_pk_add_f32 v[110:111], v[118:119], 1.0 op_sel_hi:[1,0]
	v_cvt_pk_bf16_f32 v116, v102, v103
	v_med3_f32 v102, v104, s43, v159
	v_rcp_f32_e32 v110, v110
	v_rcp_f32_e32 v111, v111
	v_med3_f32 v103, v105, s43, v159
	v_pk_add_f32 v[94:95], v[94:95], v[106:107]
	v_pk_add_f32 v[96:97], v[96:97], v[108:109]
	v_pk_mul_f32 v[104:105], v[112:113], v[110:111]
	v_min_f32_e32 v94, 0x40e00000, v94
	v_pk_mul_f32 v[102:103], v[102:103], v[104:105]
	v_min_f32_e32 v95, 0x40e00000, v95
	v_cvt_pk_bf16_f32 v117, v102, v103
	v_add_co_u32_e32 v102, vcc, s0, v146
	v_min_f32_e32 v96, 0x40e00000, v96
	s_nop 0
	v_addc_co_u32_e32 v103, vcc, 0, v147, vcc
	global_store_dwordx4 v[102:103], v[114:117], off
	v_pk_mul_f32 v[102:103], v[94:95], s[16:17] op_sel_hi:[1,0]
	v_min_f32_e32 v97, 0x40e00000, v97
	v_exp_f32_e32 v102, v102
	v_exp_f32_e32 v103, v103
	v_pk_mul_f32 v[104:105], v[96:97], s[16:17] op_sel_hi:[1,0]
	v_pk_add_f32 v[90:91], v[90:91], v[132:133]
	v_exp_f32_e32 v104, v104
	v_pk_add_f32 v[102:103], v[102:103], 1.0 op_sel_hi:[1,0]
	v_exp_f32_e32 v105, v105
	v_rcp_f32_e32 v102, v102
	v_rcp_f32_e32 v103, v103
	v_med3_f32 v90, v90, s43, v159
	v_med3_f32 v91, v91, s43, v159
	v_pk_add_f32 v[92:93], v[92:93], v[130:131]
	v_pk_mul_f32 v[94:95], v[94:95], v[102:103]
	v_med3_f32 v92, v92, s43, v159
	v_pk_mul_f32 v[90:91], v[90:91], v[94:95]
	v_pk_add_f32 v[94:95], v[104:105], 1.0 op_sel_hi:[1,0]
	v_med3_f32 v93, v93, s43, v159
	v_rcp_f32_e32 v94, v94
	v_rcp_f32_e32 v95, v95
	v_pk_add_f32 v[86:87], v[86:87], v[98:99]
	v_cvt_pk_bf16_f32 v90, v90, v91
	v_pk_add_f32 v[88:89], v[88:89], v[100:101]
	v_pk_mul_f32 v[94:95], v[96:97], v[94:95]
	v_min_f32_e32 v86, 0x40e00000, v86
	v_pk_mul_f32 v[92:93], v[92:93], v[94:95]
	v_min_f32_e32 v87, 0x40e00000, v87
	v_cvt_pk_bf16_f32 v91, v92, v93
	v_pk_mul_f32 v[92:93], v[86:87], s[16:17] op_sel_hi:[1,0]
	v_min_f32_e32 v88, 0x40e00000, v88
	v_exp_f32_e32 v92, v92
	v_exp_f32_e32 v93, v93
	v_min_f32_e32 v89, 0x40e00000, v89
	v_pk_mul_f32 v[94:95], v[88:89], s[16:17] op_sel_hi:[1,0]
	v_pk_add_f32 v[82:83], v[82:83], v[128:129]
	v_pk_add_f32 v[92:93], v[92:93], 1.0 op_sel_hi:[1,0]
	v_exp_f32_e32 v94, v94
	v_rcp_f32_e32 v92, v92
	v_rcp_f32_e32 v93, v93
	v_exp_f32_e32 v95, v95
	v_med3_f32 v82, v82, s43, v159
	v_med3_f32 v83, v83, s43, v159
	v_pk_mul_f32 v[86:87], v[86:87], v[92:93]
	v_pk_add_f32 v[84:85], v[84:85], v[126:127]
	v_pk_mul_f32 v[82:83], v[82:83], v[86:87]
	v_pk_add_f32 v[86:87], v[94:95], 1.0 op_sel_hi:[1,0]
	v_cvt_pk_bf16_f32 v92, v82, v83
	v_med3_f32 v82, v84, s43, v159
	v_rcp_f32_e32 v86, v86
	v_rcp_f32_e32 v87, v87
	v_med3_f32 v83, v85, s43, v159
	s_mov_b32 s0, 0x10000
	v_pk_add_f32 v[78:79], v[78:79], v[106:107]
	v_pk_mul_f32 v[84:85], v[88:89], v[86:87]
	v_min_f32_e32 v78, 0x40e00000, v78
	v_pk_mul_f32 v[82:83], v[82:83], v[84:85]
	v_min_f32_e32 v79, 0x40e00000, v79
	v_cvt_pk_bf16_f32 v93, v82, v83
	v_add_co_u32_e32 v82, vcc, s0, v146
	v_pk_add_f32 v[80:81], v[80:81], v[108:109]
	s_nop 0
	v_addc_co_u32_e32 v83, vcc, 0, v147, vcc
	global_store_dwordx4 v[82:83], v[90:93], off
	v_pk_mul_f32 v[82:83], v[78:79], s[16:17] op_sel_hi:[1,0]
	v_min_f32_e32 v80, 0x40e00000, v80
	v_exp_f32_e32 v82, v82
	v_exp_f32_e32 v83, v83
	v_min_f32_e32 v81, 0x40e00000, v81
	v_pk_mul_f32 v[84:85], v[80:81], s[16:17] op_sel_hi:[1,0]
	v_pk_add_f32 v[74:75], v[74:75], v[132:133]
	v_pk_add_f32 v[82:83], v[82:83], 1.0 op_sel_hi:[1,0]
	v_exp_f32_e32 v84, v84
	v_rcp_f32_e32 v82, v82
	v_rcp_f32_e32 v83, v83
	v_exp_f32_e32 v85, v85
	v_med3_f32 v74, v74, s43, v159
	v_med3_f32 v75, v75, s43, v159
	v_pk_mul_f32 v[78:79], v[78:79], v[82:83]
	v_pk_add_f32 v[76:77], v[76:77], v[130:131]
	v_pk_mul_f32 v[74:75], v[74:75], v[78:79]
	v_pk_add_f32 v[78:79], v[84:85], 1.0 op_sel_hi:[1,0]
	v_med3_f32 v76, v76, s43, v159
	v_rcp_f32_e32 v78, v78
	v_rcp_f32_e32 v79, v79
	v_med3_f32 v77, v77, s43, v159
	v_pk_add_f32 v[70:71], v[70:71], v[98:99]
	v_cvt_pk_bf16_f32 v74, v74, v75
	v_pk_mul_f32 v[78:79], v[80:81], v[78:79]
	v_min_f32_e32 v70, 0x40e00000, v70
	v_pk_mul_f32 v[76:77], v[76:77], v[78:79]
	v_min_f32_e32 v71, 0x40e00000, v71
	v_cvt_pk_bf16_f32 v75, v76, v77
	v_pk_mul_f32 v[76:77], v[70:71], s[16:17] op_sel_hi:[1,0]
	v_pk_add_f32 v[72:73], v[72:73], v[100:101]
	v_exp_f32_e32 v76, v76
	v_exp_f32_e32 v77, v77
	v_min_f32_e32 v72, 0x40e00000, v72
	v_min_f32_e32 v73, 0x40e00000, v73
	v_pk_mul_f32 v[78:79], v[72:73], s[16:17] op_sel_hi:[1,0]
	v_pk_add_f32 v[76:77], v[76:77], 1.0 op_sel_hi:[1,0]
	v_exp_f32_e32 v78, v78
	v_rcp_f32_e32 v76, v76
	v_rcp_f32_e32 v77, v77
	v_exp_f32_e32 v79, v79
	v_pk_add_f32 v[66:67], v[66:67], v[128:129]
	v_pk_add_f32 v[68:69], v[68:69], v[126:127]
	v_med3_f32 v66, v66, s43, v159
	v_med3_f32 v67, v67, s43, v159
	v_pk_mul_f32 v[70:71], v[70:71], v[76:77]
	s_mov_b32 s0, 0x18000
	v_pk_mul_f32 v[66:67], v[66:67], v[70:71]
	v_pk_add_f32 v[70:71], v[78:79], 1.0 op_sel_hi:[1,0]
	v_cvt_pk_bf16_f32 v76, v66, v67
	v_med3_f32 v66, v68, s43, v159
	v_rcp_f32_e32 v70, v70
	v_rcp_f32_e32 v71, v71
	v_med3_f32 v67, v69, s43, v159
	v_pk_add_f32 v[62:63], v[62:63], v[106:107]
	v_pk_add_f32 v[64:65], v[64:65], v[108:109]
	v_pk_mul_f32 v[68:69], v[72:73], v[70:71]
	v_min_f32_e32 v62, 0x40e00000, v62
	v_pk_mul_f32 v[66:67], v[66:67], v[68:69]
	v_min_f32_e32 v63, 0x40e00000, v63
	v_cvt_pk_bf16_f32 v77, v66, v67
	v_add_co_u32_e32 v66, vcc, s0, v146
	v_min_f32_e32 v64, 0x40e00000, v64
	s_nop 0
	v_addc_co_u32_e32 v67, vcc, 0, v147, vcc
	global_store_dwordx4 v[66:67], v[74:77], off
	v_pk_mul_f32 v[66:67], v[62:63], s[16:17] op_sel_hi:[1,0]
	v_min_f32_e32 v65, 0x40e00000, v65
; __device__ __forceinline__ unsigned cvt_pk_bf16(float lo, float hi) { unsigned r; asm volatile("v_cvt_pk_bf16_f32 %0, %1, %2" : "=v"(r) : "v"(lo), "v"(hi)); return r; }
;     __device__ __forceinline__ void operator()(const f32x4 (&acc)[2][2][4][2], const Unit& u, int wr, int wc, int fr, int fq) const {
;     ...
; #pragma unroll
;         for (int ai = 0; ai < 2; ++ai)
; #pragma unroll
;             for (int m = 0; m < 4; ++m) { unsigned wv[4];
; #pragma unroll
;                 for (int n = 0; n < 2; ++n)
; #pragma unroll
;                     for (int jp = 0; jp < 2; ++jp) {
;                         f32x2 g = (f32x2){acc[ai][0][m][n][2 * jp], acc[ai][0][m][n][2 * jp + 1]} + (f32x2){bg[n][2 * jp], bg[n][2 * jp + 1]};
;                         f32x2 uu = (f32x2){acc[ai][1][m][n][2 * jp], acc[ai][1][m][n][2 * jp + 1]} + (f32x2){bu[n][2 * jp], bu[n][2 * jp + 1]};
;                         g.x = fminf(g.x, 7.f); g.y = fminf(g.y, 7.f);
;                         uu.x = __builtin_amdgcn_fmed3f(uu.x, -6.f, 8.f); uu.y = __builtin_amdgcn_fmed3f(uu.y, -6.f, 8.f);
;                         f32x2 t = g * kk;
;                         t.x = __builtin_amdgcn_exp2f(t.x); t.y = __builtin_amdgcn_exp2f(t.y);
;                         t = t + one2;
;                         t.x = __builtin_amdgcn_rcpf(t.x); t.y = __builtin_amdgcn_rcpf(t.y);
;                         const f32x2 o = uu * (g * t);
;                         wv[n * 2 + jp] = cvt_pk_bf16(o.x, o.y); }
;                 u32x4 w; w.x = wv[0]; w.y = wv[1]; w.z = wv[2]; w.w = wv[3];
;                 *(u32x4*)(act + (size_t)(ai * HALF + m * 16) * 1024) = w; }
	v_exp_f32_e32 v66, v66
	v_exp_f32_e32 v67, v67
	v_pk_mul_f32 v[68:69], v[64:65], s[16:17] op_sel_hi:[1,0]
	v_pk_add_f32 v[58:59], v[58:59], v[132:133]
	v_exp_f32_e32 v68, v68
	v_pk_add_f32 v[66:67], v[66:67], 1.0 op_sel_hi:[1,0]
	v_exp_f32_e32 v69, v69
	v_rcp_f32_e32 v66, v66
	v_rcp_f32_e32 v67, v67
	v_med3_f32 v58, v58, s43, v159
	v_med3_f32 v59, v59, s43, v159
	v_pk_add_f32 v[60:61], v[60:61], v[130:131]
	v_pk_mul_f32 v[62:63], v[62:63], v[66:67]
	v_med3_f32 v60, v60, s43, v159
	v_pk_mul_f32 v[58:59], v[58:59], v[62:63]
	v_pk_add_f32 v[62:63], v[68:69], 1.0 op_sel_hi:[1,0]
	v_med3_f32 v61, v61, s43, v159
	v_rcp_f32_e32 v62, v62
	v_rcp_f32_e32 v63, v63
	v_pk_add_f32 v[54:55], v[54:55], v[98:99]
	v_cvt_pk_bf16_f32 v58, v58, v59
	v_pk_add_f32 v[56:57], v[56:57], v[100:101]
	v_pk_mul_f32 v[62:63], v[64:65], v[62:63]
	v_min_f32_e32 v54, 0x40e00000, v54
	v_pk_mul_f32 v[60:61], v[60:61], v[62:63]
	v_min_f32_e32 v55, 0x40e00000, v55
	v_cvt_pk_bf16_f32 v59, v60, v61
	v_pk_mul_f32 v[60:61], v[54:55], s[16:17] op_sel_hi:[1,0]
	v_min_f32_e32 v56, 0x40e00000, v56
	v_exp_f32_e32 v60, v60
	v_exp_f32_e32 v61, v61
	v_min_f32_e32 v57, 0x40e00000, v57
	v_pk_mul_f32 v[62:63], v[56:57], s[16:17] op_sel_hi:[1,0]
	v_pk_add_f32 v[50:51], v[50:51], v[128:129]
	v_pk_add_f32 v[60:61], v[60:61], 1.0 op_sel_hi:[1,0]
	v_exp_f32_e32 v62, v62
	v_rcp_f32_e32 v60, v60
	v_rcp_f32_e32 v61, v61
	v_exp_f32_e32 v63, v63
	v_med3_f32 v50, v50, s43, v159
	v_med3_f32 v51, v51, s43, v159
	v_pk_mul_f32 v[54:55], v[54:55], v[60:61]
	v_pk_add_f32 v[52:53], v[52:53], v[126:127]
	v_pk_mul_f32 v[50:51], v[50:51], v[54:55]
	v_pk_add_f32 v[54:55], v[62:63], 1.0 op_sel_hi:[1,0]
	v_cvt_pk_bf16_f32 v60, v50, v51
	v_med3_f32 v50, v52, s43, v159
	v_rcp_f32_e32 v54, v54
	v_rcp_f32_e32 v55, v55
	v_med3_f32 v51, v53, s43, v159
	v_pk_add_f32 v[46:47], v[46:47], v[106:107]
	v_pk_add_f32 v[48:49], v[48:49], v[108:109]
	v_pk_mul_f32 v[52:53], v[56:57], v[54:55]
	v_min_f32_e32 v46, 0x40e00000, v46
	v_pk_mul_f32 v[50:51], v[50:51], v[52:53]
	v_min_f32_e32 v47, 0x40e00000, v47
	v_cvt_pk_bf16_f32 v61, v50, v51
	v_add_co_u32_e32 v50, vcc, s44, v146
	v_min_f32_e32 v48, 0x40e00000, v48
	s_nop 0
	v_addc_co_u32_e32 v51, vcc, 0, v147, vcc
	global_store_dwordx4 v[50:51], v[58:61], off
	v_pk_mul_f32 v[50:51], v[46:47], s[16:17] op_sel_hi:[1,0]
	v_min_f32_e32 v49, 0x40e00000, v49
	v_exp_f32_e32 v50, v50
	v_exp_f32_e32 v51, v51
	v_pk_mul_f32 v[52:53], v[48:49], s[16:17] op_sel_hi:[1,0]
	v_pk_add_f32 v[42:43], v[42:43], v[132:133]
	v_exp_f32_e32 v52, v52
	v_pk_add_f32 v[50:51], v[50:51], 1.0 op_sel_hi:[1,0]
	v_exp_f32_e32 v53, v53
	v_rcp_f32_e32 v50, v50
	v_rcp_f32_e32 v51, v51
	v_med3_f32 v42, v42, s43, v159
	v_med3_f32 v43, v43, s43, v159
	v_pk_add_f32 v[44:45], v[44:45], v[130:131]
	v_pk_mul_f32 v[46:47], v[46:47], v[50:51]
	v_med3_f32 v44, v44, s43, v159
	v_pk_mul_f32 v[42:43], v[42:43], v[46:47]
	v_pk_add_f32 v[46:47], v[52:53], 1.0 op_sel_hi:[1,0]
	v_med3_f32 v45, v45, s43, v159
	v_rcp_f32_e32 v46, v46
	v_rcp_f32_e32 v47, v47
	v_pk_add_f32 v[38:39], v[38:39], v[98:99]
	v_cvt_pk_bf16_f32 v42, v42, v43
	v_pk_add_f32 v[40:41], v[40:41], v[100:101]
	v_pk_mul_f32 v[46:47], v[48:49], v[46:47]
	v_min_f32_e32 v38, 0x40e00000, v38
	v_pk_mul_f32 v[44:45], v[44:45], v[46:47]
	v_min_f32_e32 v39, 0x40e00000, v39
	v_cvt_pk_bf16_f32 v43, v44, v45
	v_pk_mul_f32 v[44:45], v[38:39], s[16:17] op_sel_hi:[1,0]
	v_min_f32_e32 v40, 0x40e00000, v40
	v_exp_f32_e32 v44, v44
	v_exp_f32_e32 v45, v45
	v_min_f32_e32 v41, 0x40e00000, v41
	v_pk_mul_f32 v[46:47], v[40:41], s[16:17] op_sel_hi:[1,0]
	v_pk_add_f32 v[34:35], v[34:35], v[128:129]
	v_pk_add_f32 v[44:45], v[44:45], 1.0 op_sel_hi:[1,0]
	v_exp_f32_e32 v46, v46
	v_rcp_f32_e32 v44, v44
	v_rcp_f32_e32 v45, v45
	v_exp_f32_e32 v47, v47
	v_med3_f32 v34, v34, s43, v159
	v_med3_f32 v35, v35, s43, v159
	v_pk_mul_f32 v[38:39], v[38:39], v[44:45]
	v_pk_add_f32 v[36:37], v[36:37], v[126:127]
	v_pk_mul_f32 v[34:35], v[34:35], v[38:39]
	v_pk_add_f32 v[38:39], v[46:47], 1.0 op_sel_hi:[1,0]
	v_cvt_pk_bf16_f32 v44, v34, v35
	v_med3_f32 v34, v36, s43, v159
	v_rcp_f32_e32 v38, v38
	v_rcp_f32_e32 v39, v39
	v_med3_f32 v35, v37, s43, v159
	v_pk_add_f32 v[30:31], v[30:31], v[106:107]
	v_pk_add_f32 v[32:33], v[32:33], v[108:109]
	v_pk_mul_f32 v[36:37], v[40:41], v[38:39]
	v_min_f32_e32 v30, 0x40e00000, v30
	v_pk_mul_f32 v[34:35], v[34:35], v[36:37]
	v_min_f32_e32 v31, 0x40e00000, v31
	v_cvt_pk_bf16_f32 v45, v34, v35
	v_add_co_u32_e32 v34, vcc, s45, v146
	v_min_f32_e32 v32, 0x40e00000, v32
	s_nop 0
	v_addc_co_u32_e32 v35, vcc, 0, v147, vcc
	global_store_dwordx4 v[34:35], v[42:45], off
	v_pk_mul_f32 v[34:35], v[30:31], s[16:17] op_sel_hi:[1,0]
	v_min_f32_e32 v33, 0x40e00000, v33
; __device__ __forceinline__ unsigned cvt_pk_bf16(float lo, float hi) { unsigned r; asm volatile("v_cvt_pk_bf16_f32 %0, %1, %2" : "=v"(r) : "v"(lo), "v"(hi)); return r; }
; template <class Epi, class Sched, bool GATHER, bool ALIGN_EPI, bool PFB = false>
; __device__ __forceinline__ void gemm_phase(LAS unsigned char* lds, const int lda, const int K, const Sched& S, const Epi& E) {
;     ...
;         if (!has_next) break;
; #pragma unroll
;         for (int a = 0; a < 2; ++a)
; #pragma unroll
;             for (int b = 0; b < 2; ++b)
; #pragma unroll
;                 for (int m = 0; m < 4; ++m)
; #pragma unroll
;                     for (int n = 0; n < 2; ++n) acc[a][b][m][n] = (f32x4){0.f, 0.f, 0.f, 0.f};
;         cur = nxt; cA = nA; cB = nB; ++ui;
;         if (GATHER) {
; #pragma unroll
;             for (int i = 0; i < 2; ++i) { vA0[i] = nA0[i]; vA1[i] = nA1[i]; }
;         }
;         if constexpr (ALIGN_EPI) { if (wr == 1) G8_BAR; }
;     }
;     __device__ __forceinline__ void operator()(const f32x4 (&acc)[2][2][4][2], const Unit& u, int wr, int wc, int fr, int fq) const {
;     ...
; #pragma unroll
;         for (int ai = 0; ai < 2; ++ai)
; #pragma unroll
;             for (int m = 0; m < 4; ++m) { unsigned wv[4];
; #pragma unroll
;                 for (int n = 0; n < 2; ++n)
; #pragma unroll
;                     for (int jp = 0; jp < 2; ++jp) {
;                         f32x2 g = (f32x2){acc[ai][0][m][n][2 * jp], acc[ai][0][m][n][2 * jp + 1]} + (f32x2){bg[n][2 * jp], bg[n][2 * jp + 1]};
;                         f32x2 uu = (f32x2){acc[ai][1][m][n][2 * jp], acc[ai][1][m][n][2 * jp + 1]} + (f32x2){bu[n][2 * jp], bu[n][2 * jp + 1]};
;                         g.x = fminf(g.x, 7.f); g.y = fminf(g.y, 7.f);
;                         uu.x = __builtin_amdgcn_fmed3f(uu.x, -6.f, 8.f); uu.y = __builtin_amdgcn_fmed3f(uu.y, -6.f, 8.f);
;                         f32x2 t = g * kk;
;                         t.x = __builtin_amdgcn_exp2f(t.x); t.y = __builtin_amdgcn_exp2f(t.y);
;                         t = t + one2;
;                         t.x = __builtin_amdgcn_rcpf(t.x); t.y = __builtin_amdgcn_rcpf(t.y);
;                         const f32x2 o = uu * (g * t);
;                         wv[n * 2 + jp] = cvt_pk_bf16(o.x, o.y); }
;                 u32x4 w; w.x = wv[0]; w.y = wv[1]; w.z = wv[2]; w.w = wv[3];
;                 *(u32x4*)(act + (size_t)(ai * HALF + m * 16) * 1024) = w; }
	v_exp_f32_e32 v34, v34
	v_exp_f32_e32 v35, v35
	v_pk_mul_f32 v[36:37], v[32:33], s[16:17] op_sel_hi:[1,0]
	v_pk_add_f32 v[26:27], v[26:27], v[132:133]
	v_exp_f32_e32 v36, v36
	v_pk_add_f32 v[34:35], v[34:35], 1.0 op_sel_hi:[1,0]
	v_exp_f32_e32 v37, v37
	v_rcp_f32_e32 v34, v34
	v_rcp_f32_e32 v35, v35
	v_med3_f32 v26, v26, s43, v159
	v_med3_f32 v27, v27, s43, v159
	v_pk_add_f32 v[28:29], v[28:29], v[130:131]
	v_pk_mul_f32 v[30:31], v[30:31], v[34:35]
	v_med3_f32 v28, v28, s43, v159
	v_pk_mul_f32 v[26:27], v[26:27], v[30:31]
	v_pk_add_f32 v[30:31], v[36:37], 1.0 op_sel_hi:[1,0]
	v_med3_f32 v29, v29, s43, v159
	v_rcp_f32_e32 v30, v30
	v_rcp_f32_e32 v31, v31
	v_pk_add_f32 v[22:23], v[22:23], v[98:99]
	v_cvt_pk_bf16_f32 v26, v26, v27
	v_pk_add_f32 v[24:25], v[24:25], v[100:101]
	v_pk_mul_f32 v[30:31], v[32:33], v[30:31]
	v_min_f32_e32 v22, 0x40e00000, v22
	v_pk_mul_f32 v[28:29], v[28:29], v[30:31]
	v_min_f32_e32 v23, 0x40e00000, v23
	v_cvt_pk_bf16_f32 v27, v28, v29
	v_pk_mul_f32 v[28:29], v[22:23], s[16:17] op_sel_hi:[1,0]
	v_min_f32_e32 v24, 0x40e00000, v24
	v_exp_f32_e32 v28, v28
	v_exp_f32_e32 v29, v29
	v_min_f32_e32 v25, 0x40e00000, v25
	v_pk_mul_f32 v[30:31], v[24:25], s[16:17] op_sel_hi:[1,0]
	v_pk_add_f32 v[18:19], v[18:19], v[128:129]
	v_pk_add_f32 v[28:29], v[28:29], 1.0 op_sel_hi:[1,0]
	v_exp_f32_e32 v30, v30
	v_rcp_f32_e32 v28, v28
	v_rcp_f32_e32 v29, v29
	v_exp_f32_e32 v31, v31
	v_med3_f32 v18, v18, s43, v159
	v_med3_f32 v19, v19, s43, v159
	v_pk_mul_f32 v[22:23], v[22:23], v[28:29]
	v_pk_add_f32 v[20:21], v[20:21], v[126:127]
	v_pk_mul_f32 v[18:19], v[18:19], v[22:23]
	v_pk_add_f32 v[22:23], v[30:31], 1.0 op_sel_hi:[1,0]
	v_cvt_pk_bf16_f32 v28, v18, v19
	v_med3_f32 v18, v20, s43, v159
	v_rcp_f32_e32 v22, v22
	v_rcp_f32_e32 v23, v23
	v_med3_f32 v19, v21, s43, v159
	v_pk_add_f32 v[14:15], v[14:15], v[106:107]
	v_pk_add_f32 v[16:17], v[16:17], v[108:109]
	v_pk_mul_f32 v[20:21], v[24:25], v[22:23]
	v_min_f32_e32 v14, 0x40e00000, v14
	v_pk_mul_f32 v[18:19], v[18:19], v[20:21]
	v_min_f32_e32 v15, 0x40e00000, v15
	v_cvt_pk_bf16_f32 v29, v18, v19
	v_add_co_u32_e32 v18, vcc, s46, v146
	v_min_f32_e32 v16, 0x40e00000, v16
	s_nop 0
	v_addc_co_u32_e32 v19, vcc, 0, v147, vcc
	global_store_dwordx4 v[18:19], v[26:29], off
	v_pk_mul_f32 v[18:19], v[14:15], s[16:17] op_sel_hi:[1,0]
	v_min_f32_e32 v17, 0x40e00000, v17
	v_exp_f32_e32 v18, v18
	v_exp_f32_e32 v19, v19
	v_pk_mul_f32 v[20:21], v[16:17], s[16:17] op_sel_hi:[1,0]
	v_pk_add_f32 v[10:11], v[10:11], v[132:133]
	v_exp_f32_e32 v20, v20
	v_pk_add_f32 v[18:19], v[18:19], 1.0 op_sel_hi:[1,0]
	v_exp_f32_e32 v21, v21
	v_rcp_f32_e32 v18, v18
	v_rcp_f32_e32 v19, v19
	v_med3_f32 v10, v10, s43, v159
	v_med3_f32 v11, v11, s43, v159
	v_pk_add_f32 v[12:13], v[12:13], v[130:131]
	v_pk_mul_f32 v[14:15], v[14:15], v[18:19]
	v_med3_f32 v12, v12, s43, v159
	v_pk_mul_f32 v[10:11], v[10:11], v[14:15]
	v_pk_add_f32 v[14:15], v[20:21], 1.0 op_sel_hi:[1,0]
	v_med3_f32 v13, v13, s43, v159
	v_rcp_f32_e32 v14, v14
	v_rcp_f32_e32 v15, v15
	v_pk_add_f32 v[6:7], v[6:7], v[98:99]
	v_cvt_pk_bf16_f32 v10, v10, v11
	v_pk_add_f32 v[8:9], v[8:9], v[100:101]
	v_pk_mul_f32 v[14:15], v[16:17], v[14:15]
	v_min_f32_e32 v6, 0x40e00000, v6
	v_pk_mul_f32 v[12:13], v[12:13], v[14:15]
	v_min_f32_e32 v7, 0x40e00000, v7
	v_cvt_pk_bf16_f32 v11, v12, v13
	v_pk_mul_f32 v[12:13], v[6:7], s[16:17] op_sel_hi:[1,0]
	v_min_f32_e32 v8, 0x40e00000, v8
	v_exp_f32_e32 v12, v12
	v_exp_f32_e32 v13, v13
	v_min_f32_e32 v9, 0x40e00000, v9
	v_pk_mul_f32 v[14:15], v[8:9], s[16:17] op_sel_hi:[1,0]
	v_pk_add_f32 v[2:3], v[2:3], v[128:129]
	v_pk_add_f32 v[12:13], v[12:13], 1.0 op_sel_hi:[1,0]
	v_exp_f32_e32 v14, v14
	v_rcp_f32_e32 v12, v12
	v_rcp_f32_e32 v13, v13
	v_exp_f32_e32 v15, v15
	v_med3_f32 v2, v2, s43, v159
	v_med3_f32 v3, v3, s43, v159
	v_pk_mul_f32 v[6:7], v[6:7], v[12:13]
	v_pk_add_f32 v[4:5], v[4:5], v[126:127]
	v_pk_mul_f32 v[2:3], v[2:3], v[6:7]
	v_pk_add_f32 v[6:7], v[14:15], 1.0 op_sel_hi:[1,0]
	v_cvt_pk_bf16_f32 v12, v2, v3
	v_med3_f32 v2, v4, s43, v159
	v_rcp_f32_e32 v6, v6
	v_rcp_f32_e32 v7, v7
	v_med3_f32 v3, v5, s43, v159
	s_mov_b64 s[0:1], -1
	v_pk_mul_f32 v[4:5], v[8:9], v[6:7]
	s_nop 0
	v_pk_mul_f32 v[2:3], v[2:3], v[4:5]
	s_nop 0
	v_cvt_pk_bf16_f32 v13, v2, v3
	v_add_co_u32_e32 v2, vcc, 0x58000, v146
	s_nop 1
	v_addc_co_u32_e32 v3, vcc, 0, v147, vcc
	s_and_b64 vcc, exec, s[4:5]
	global_store_dwordx4 v[2:3], v[10:13], off
	s_cbranch_vccnz .LBB0_1494
	s_andn2_b64 vcc, exec, s[6:7]
	s_cbranch_vccnz .LBB0_1493
	s_barrier
	s_branch .LBB0_1493
.LBB0_1510:
	v_and_b32_e32 v182, 63, v0
	v_lshl_add_u32 v183, v0, 2, 0
	v_and_b32_e32 v184, 31, v0
	v_bfe_u32 v185, v0, 4, 2
	s_waitcnt vmcnt(0)
	s_barrier

;     __device__ __forceinline__ bool next(int i, Unit& u) const {
;         const int L = i * G + vcu;
;         if (L >= tab[96]) return false;
;         const int me = threadIdx.x & 31;
;         const int st_l = tab[me], c_l = tab[32 + me];
;         const unsigned long long m = __ballot(L >= st_l && L < st_l + ((c_l + 255) >> 8) * nN);
;         const int e = __builtin_amdgcn_readfirstlane(__builtin_ctzll(m) & 31);
;         const int st = tab[e], c = tab[32 + e], ab = tab[64 + e];
;         const int l = L - st;
;         const int sh = nN == 8 ? 3 : 2;
;         u.e = e; u.pm = l >> sh; u.pn = l & (nN - 1); u.aux = ab; u.cnt = c;
;         u.a = gather ? Abase : Abase + (size_t)(ab + u.pm * 256) * 1024 * 2; u.b = Bbase + (size_t)e * bstride + (size_t)u.pn * 256 * K * 2; return true;
;     __device__ __forceinline__ void operator()(const f32x4 (&acc)[2][2][4][2], const Unit& u, int wr, int wc, int fr, int fq) const {
;     ...
;         const float* bgu = P.in[35] + (size_t)(layer * NE + u.e) * 2048;
;         const int cl = u.pn * 128 + wc * 32 + 8 * fq;
;         f32x4 bg[2], bu[2];
; #pragma unroll
;         for (int n = 0; n < 2; ++n) { bg[n] = *(const f32x4*)(bgu + cl + 4 * n); bu[n] = *(const f32x4*)(bgu + 1024 + cl + 4 * n) + 1.f; }
.LBB0_2357:
	s_lshl_b32 s32, s24, 13
	v_mov_b32_e32 v16, s32
	v_mov_b32_e32 v17, 0
	v_lshl_add_u64 v[16:17], v[16:17], 0, s[70:71]
	v_lshl_or_b32 v18, s60, 7, v158
	v_ashrrev_i32_e32 v19, 31, v18
	v_lshl_add_u64 v[20:21], v[18:19], 2, v[16:17]
	v_lshl_add_u64 v[22:23], v[20:21], 0, s[16:17]
	v_lshl_add_u64 v[24:25], v[20:21], 0, s[18:19]
	v_mov_b32_e32 v26, s50
	v_mov_b32_e32 v27, 0
	v_lshl_add_u64 v[26:27], v[26:27], 0, v[20:21]
	global_load_dwordx4 v[240:243], v[22:23], off offset:16
	global_load_dwordx4 v[244:247], v[24:25], off offset:16
	global_load_dwordx4 v[248:251], v[26:27], off
	global_load_dwordx4 v[182:185], v[26:27], off offset:-4096
	ds_read_b32 v2, v159
	s_add_i32 s44, s44, 1
	s_mul_i32 s25, s44, s62
	v_readlane_b32 s0, v254, 2
	s_add_i32 s25, s25, s0
	s_waitcnt lgkmcnt(0)
	v_cmp_ge_i32_e32 vcc, s25, v2
	v_cmp_lt_i32_e64 s[0:1], s25, v2
	s_cbranch_vccnz .LBB0_2361
	ds_read_b32 v2, v152
	s_mov_b64 s[22:23], 0
	s_waitcnt lgkmcnt(0)
	v_cmp_ge_i32_e32 vcc, s25, v2
	s_and_saveexec_b64 s[4:5], vcc
	s_cbranch_execz .LBB0_2360
	ds_read_b32 v3, v152 offset:128
	s_waitcnt lgkmcnt(0)
	v_add_u32_e32 v3, 0xff, v3
	v_ashrrev_i32_e32 v3, 5, v3
	v_and_b32_e32 v3, -8, v3
	v_add_u32_e32 v2, v3, v2
	v_cmp_lt_i32_e32 vcc, s25, v2
	s_and_b64 s[22:23], vcc, exec

; template <class Epi, class Sched, bool GATHER, bool ALIGN_EPI, bool PFB = false>
; __device__ __forceinline__ void gemm_phase(LAS unsigned char* lds, const int lda, const int K, const Sched& S, const Epi& E) {
;     ...
;         if (GATHER) {
; #pragma unroll
;             for (int i = 0; i < 2; ++i) { if (has_next) { nA0[i] = S.arow_off(nxt, Rr[i]) + (unsigned)Cc[i] * 2u; nA1[i] = S.arow_off(nxt, HALF + Rr[i]) + (unsigned)Cc[i] * 2u; } else { nA0[i] = vA0[i]; nA1[i] = vA1[i]; } }
;         }
;     __device__ __forceinline__ unsigned arow_off(const Unit& u, int r) const { int rr = u.pm * 256 + r; rr = rr < u.cnt ? rr : u.cnt - 1; return (unsigned)rowtab[(size_t)u.e * R + rr] * (unsigned)(D * 2); }
.LBB0_2361:
	s_lshl_b32 s25, s56, 8
	s_mul_i32 s5, s54, 0x11000
	s_mul_hi_i32 s4, s54, 0x11000
	s_add_u32 s28, s35, s5
	v_cndmask_b32_e64 v3, 0, 1, s[0:1]
	v_add_u32_e32 v2, -1, v145
	s_addc_u32 s29, s36, s4
	s_or_b32 s30, s25, 0x80
	v_cmp_ne_u32_e64 s[4:5], 1, v3
	s_andn2_b64 vcc, exec, s[0:1]
	v_mov_b32_e32 v144, v99
	v_mov_b32_e32 v165, v100
	s_cbranch_vccnz .LBB0_2363
	v_or_b32_e32 v3, s25, v153
	v_min_i32_e32 v4, v3, v2
	v_or_b32_e32 v3, s30, v153
	v_ashrrev_i32_e32 v5, 31, v4
	v_min_i32_e32 v6, v3, v2
	v_lshl_add_u64 v[4:5], v[4:5], 2, s[28:29]
	v_ashrrev_i32_e32 v7, 31, v6
	v_lshl_add_u64 v[6:7], v[6:7], 2, s[28:29]
	v_or_b32_e32 v8, s25, v154
	v_min_i32_e32 v8, v8, v2
	v_add_u32_e32 v10, s30, v154
	v_min_i32_e32 v10, v10, v2
	v_ashrrev_i32_e32 v9, 31, v8
	v_ashrrev_i32_e32 v11, 31, v10
	v_lshl_add_u64 v[8:9], v[8:9], 2, s[28:29]
	v_lshl_add_u64 v[10:11], v[10:11], 2, s[28:29]
	global_load_dword v12, v[4:5], off
	global_load_dword v13, v[6:7], off
	global_load_dword v14, v[8:9], off
	global_load_dword v15, v[10:11], off
	s_waitcnt vmcnt(0)
	v_lshl_or_b32 v144, v12, 11, v155
	v_lshl_or_b32 v165, v13, 11, v155
.LBB0_2363:
	s_and_b64 vcc, exec, s[4:5]
	v_mov_b32_e32 v166, v98
	v_mov_b32_e32 v167, v110
	s_cbranch_vccnz .LBB0_2365
	v_lshl_or_b32 v166, v14, 11, v155
	v_lshl_or_b32 v167, v15, 11, v155

; __device__ __forceinline__ unsigned cvt_pk_bf16(float lo, float hi) { unsigned r; asm volatile("v_cvt_pk_bf16_f32 %0, %1, %2" : "=v"(r) : "v"(lo), "v"(hi)); return r; }
;     __device__ __forceinline__ void operator()(const f32x4 (&acc)[2][2][4][2], const Unit& u, int wr, int wc, int fr, int fq) const {
;     ...
;         const float* bgu = P.in[35] + (size_t)(layer * NE + u.e) * 2048;
;         const int cl = u.pn * 128 + wc * 32 + 8 * fq;
;         f32x4 bg[2], bu[2];
; #pragma unroll
;         for (int n = 0; n < 2; ++n) { bg[n] = *(const f32x4*)(bgu + cl + 4 * n); bu[n] = *(const f32x4*)(bgu + 1024 + cl + 4 * n) + 1.f; }
;         bf16* act = (bf16*)(P.ws + WS_ACT) + (size_t)(u.aux + u.pm * 256 + wr * 64 + fr) * 1024 + cl;
;         const f32x2 kk = {-1.702f * LOG2E, -1.702f * LOG2E}, one2 = {1.f, 1.f};
; #pragma unroll
;         for (int ai = 0; ai < 2; ++ai)
; #pragma unroll
;             for (int m = 0; m < 4; ++m) { unsigned wv[4];
; #pragma unroll
;                 for (int n = 0; n < 2; ++n)
; #pragma unroll
;                     for (int jp = 0; jp < 2; ++jp) {
;                         f32x2 g = (f32x2){acc[ai][0][m][n][2 * jp], acc[ai][0][m][n][2 * jp + 1]} + (f32x2){bg[n][2 * jp], bg[n][2 * jp + 1]};
;                         f32x2 uu = (f32x2){acc[ai][1][m][n][2 * jp], acc[ai][1][m][n][2 * jp + 1]} + (f32x2){bu[n][2 * jp], bu[n][2 * jp + 1]};
;                         g.x = fminf(g.x, 7.f); g.y = fminf(g.y, 7.f);
;                         uu.x = __builtin_amdgcn_fmed3f(uu.x, -6.f, 8.f); uu.y = __builtin_amdgcn_fmed3f(uu.y, -6.f, 8.f);
;                         f32x2 t = g * kk;
;                         t.x = __builtin_amdgcn_exp2f(t.x); t.y = __builtin_amdgcn_exp2f(t.y);
;                         t = t + one2;
;                         t.x = __builtin_amdgcn_rcpf(t.x); t.y = __builtin_amdgcn_rcpf(t.y);
;                         const f32x2 o = uu * (g * t);
;                         wv[n * 2 + jp] = cvt_pk_bf16(o.x, o.y); }
;                 u32x4 w; w.x = wv[0]; w.y = wv[1]; w.z = wv[2]; w.w = wv[3];
;                 *(u32x4*)(act + (size_t)(ai * HALF + m * 16) * 1024) = w; }
.LBB0_2369:
	s_ashr_i32 s25, s24, 31
	s_lshl_b64 s[0:1], s[24:25], 13
	s_add_u32 s0, s70, s0
	v_lshl_or_b32 v146, s60, 7, v158
	s_addc_u32 s1, s71, s1
	v_ashrrev_i32_e32 v147, 31, v146
	v_lshl_add_u64 v[110:111], v[146:147], 2, s[0:1]
	v_lshl_add_u64 v[98:99], v[110:111], 0, s[16:17]
	v_lshl_add_u64 v[112:113], v[110:111], 0, s[18:19]
	v_add_co_u32_e32 v110, vcc, s50, v110
	v_addc_co_u32_e32 v111, vcc, 0, v111, vcc
	s_lshl_b32 s0, s57, 8
	v_add_u32_e32 v142, s0, v148
	v_add_u32_e32 v148, v142, v156
	v_ashrrev_i32_e32 v149, 31, v148
	v_lshlrev_b64 v[148:149], 11, v[148:149]
	v_lshl_add_u64 v[148:149], s[12:13], 0, v[148:149]
	v_lshl_add_u64 v[146:147], v[146:147], 1, v[148:149]
	s_mov_b64 s[0:1], -1
	v_mov_b64_e32 v[98:99], v[240:241]
	v_mov_b64_e32 v[100:101], v[242:243]
	v_mov_b64_e32 v[168:169], v[244:245]
	v_mov_b64_e32 v[170:171], v[246:247]
	v_mov_b64_e32 v[172:173], v[248:249]
	v_mov_b64_e32 v[174:175], v[250:251]
	v_mov_b64_e32 v[110:111], v[182:183]
	v_mov_b64_e32 v[112:113], v[184:185]
	v_pk_add_f32 v[106:107], v[106:107], v[98:99]
	v_pk_add_f32 v[148:149], v[170:171], 1.0 op_sel_hi:[1,0]
	v_pk_add_f32 v[150:151], v[168:169], 1.0 op_sel_hi:[1,0]
	v_pk_add_f32 v[168:169], v[132:133], v[100:101]
	v_pk_add_f32 v[170:171], v[130:131], v[98:99]
	v_pk_add_f32 v[130:131], v[174:175], 1.0 op_sel_hi:[1,0]
	v_pk_add_f32 v[132:133], v[172:173], 1.0 op_sel_hi:[1,0]
	v_pk_add_f32 v[136:137], v[136:137], v[112:113]
	v_pk_add_f32 v[134:135], v[134:135], v[110:111]
	v_pk_add_f32 v[120:121], v[120:121], v[130:131]
	v_pk_add_f32 v[118:119], v[118:119], v[132:133]
	v_min_f32_e32 v134, 0x40e00000, v134
	v_min_f32_e32 v135, 0x40e00000, v135
	v_min_f32_e32 v136, 0x40e00000, v136
	v_min_f32_e32 v137, 0x40e00000, v137
	v_min_f32_e32 v170, 0x40e00000, v170
	v_min_f32_e32 v171, 0x40e00000, v171
	v_min_f32_e32 v168, 0x40e00000, v168
	v_min_f32_e32 v169, 0x40e00000, v169
	v_pk_add_f32 v[176:177], v[116:117], v[130:131]
	v_pk_add_f32 v[178:179], v[114:115], v[132:133]
	v_med3_f32 v114, v118, s51, v163
	v_med3_f32 v115, v119, s51, v163
	v_pk_mul_f32 v[116:117], v[134:135], s[20:21] op_sel_hi:[1,0]
	v_med3_f32 v118, v120, s51, v163
	v_med3_f32 v119, v121, s51, v163
	v_pk_mul_f32 v[120:121], v[136:137], s[20:21] op_sel_hi:[1,0]
	v_pk_mul_f32 v[172:173], v[170:171], s[20:21] op_sel_hi:[1,0]
	v_pk_mul_f32 v[174:175], v[168:169], s[20:21] op_sel_hi:[1,0]
	v_exp_f32_e32 v116, v116
	v_exp_f32_e32 v117, v117
	v_exp_f32_e32 v120, v120
	v_exp_f32_e32 v121, v121
	v_exp_f32_e32 v172, v172
	v_exp_f32_e32 v173, v173
	v_exp_f32_e32 v174, v174
	v_exp_f32_e32 v175, v175
	v_pk_add_f32 v[116:117], v[116:117], 1.0 op_sel_hi:[1,0]
	v_pk_add_f32 v[120:121], v[120:121], 1.0 op_sel_hi:[1,0]
	v_pk_add_f32 v[172:173], v[172:173], 1.0 op_sel_hi:[1,0]
	v_pk_add_f32 v[174:175], v[174:175], 1.0 op_sel_hi:[1,0]
	v_rcp_f32_e32 v116, v116
	v_rcp_f32_e32 v117, v117
	v_rcp_f32_e32 v120, v120
	v_rcp_f32_e32 v121, v121
	v_rcp_f32_e32 v172, v172
	v_rcp_f32_e32 v173, v173
	v_rcp_f32_e32 v174, v174
	v_rcp_f32_e32 v175, v175
	v_pk_add_f32 v[128:129], v[128:129], v[148:149]
	v_pk_add_f32 v[126:127], v[126:127], v[150:151]
	v_pk_add_f32 v[122:123], v[122:123], v[110:111]
	v_pk_mul_f32 v[116:117], v[134:135], v[116:117]
	v_pk_mul_f32 v[120:121], v[136:137], v[120:121]
	v_med3_f32 v126, v126, s51, v163
	v_med3_f32 v127, v127, s51, v163
	v_med3_f32 v128, v128, s51, v163
	v_med3_f32 v129, v129, s51, v163
	v_min_f32_e32 v122, 0x40e00000, v122
	v_min_f32_e32 v123, 0x40e00000, v123
	v_pk_mul_f32 v[170:171], v[170:171], v[172:173]
	v_pk_mul_f32 v[168:169], v[168:169], v[174:175]
	v_pk_mul_f32 v[114:115], v[114:115], v[116:117]
	v_pk_mul_f32 v[116:117], v[118:119], v[120:121]
	v_pk_add_f32 v[124:125], v[124:125], v[112:113]
	v_pk_mul_f32 v[180:181], v[122:123], s[20:21] op_sel_hi:[1,0]
	v_pk_mul_f32 v[126:127], v[126:127], v[170:171]
	v_pk_mul_f32 v[128:129], v[128:129], v[168:169]
	v_cvt_pk_bf16_f32 v114, v114, v115
	v_cvt_pk_bf16_f32 v115, v116, v117
	v_cvt_pk_bf16_f32 v116, v126, v127
	v_exp_f32_e32 v180, v180
	v_cvt_pk_bf16_f32 v117, v128, v129
	v_exp_f32_e32 v181, v181
	global_store_dwordx4 v[146:147], v[114:117], off
	v_med3_f32 v178, v178, s51, v163
	v_med3_f32 v179, v179, s51, v163
	v_min_f32_e32 v116, 0x40e00000, v124
	v_min_f32_e32 v117, 0x40e00000, v125
	v_pk_mul_f32 v[114:115], v[116:117], s[20:21] op_sel_hi:[1,0]
	v_pk_add_f32 v[180:181], v[180:181], 1.0 op_sel_hi:[1,0]
	v_exp_f32_e32 v114, v114
	v_exp_f32_e32 v115, v115
	v_rcp_f32_e32 v180, v180
	v_rcp_f32_e32 v181, v181
	v_min_f32_e32 v106, 0x40e00000, v106
	v_pk_add_f32 v[114:115], v[114:115], 1.0 op_sel_hi:[1,0]
	v_min_f32_e32 v107, 0x40e00000, v107
	v_rcp_f32_e32 v120, v114
	v_rcp_f32_e32 v121, v115
	v_pk_mul_f32 v[118:119], v[122:123], v[180:181]
	v_pk_add_f32 v[108:109], v[108:109], v[100:101]
	v_pk_mul_f32 v[118:119], v[178:179], v[118:119]
	v_pk_mul_f32 v[116:117], v[116:117], v[120:121]
	v_cvt_pk_bf16_f32 v114, v118, v119
	v_med3_f32 v118, v176, s51, v163
	v_med3_f32 v119, v177, s51, v163
	v_pk_mul_f32 v[116:117], v[118:119], v[116:117]
	v_min_f32_e32 v108, 0x40e00000, v108
	v_cvt_pk_bf16_f32 v115, v116, v117
	v_pk_mul_f32 v[116:117], v[106:107], s[20:21] op_sel_hi:[1,0]
	v_min_f32_e32 v109, 0x40e00000, v109
	v_exp_f32_e32 v116, v116
	v_exp_f32_e32 v117, v117
	v_pk_mul_f32 v[118:119], v[108:109], s[20:21] op_sel_hi:[1,0]
	v_pk_add_f32 v[102:103], v[102:103], v[150:151]
	v_exp_f32_e32 v118, v118
	v_pk_add_f32 v[116:117], v[116:117], 1.0 op_sel_hi:[1,0]
	v_exp_f32_e32 v119, v119
	v_rcp_f32_e32 v116, v116
	v_rcp_f32_e32 v117, v117
	v_med3_f32 v102, v102, s51, v163
	v_med3_f32 v103, v103, s51, v163
	v_pk_add_f32 v[104:105], v[104:105], v[148:149]
; __device__ __forceinline__ unsigned cvt_pk_bf16(float lo, float hi) { unsigned r; asm volatile("v_cvt_pk_bf16_f32 %0, %1, %2" : "=v"(r) : "v"(lo), "v"(hi)); return r; }
;     __device__ __forceinline__ void operator()(const f32x4 (&acc)[2][2][4][2], const Unit& u, int wr, int wc, int fr, int fq) const {
;     ...
; #pragma unroll
;         for (int ai = 0; ai < 2; ++ai)
; #pragma unroll
;             for (int m = 0; m < 4; ++m) { unsigned wv[4];
; #pragma unroll
;                 for (int n = 0; n < 2; ++n)
; #pragma unroll
;                     for (int jp = 0; jp < 2; ++jp) {
;                         f32x2 g = (f32x2){acc[ai][0][m][n][2 * jp], acc[ai][0][m][n][2 * jp + 1]} + (f32x2){bg[n][2 * jp], bg[n][2 * jp + 1]};
;                         f32x2 uu = (f32x2){acc[ai][1][m][n][2 * jp], acc[ai][1][m][n][2 * jp + 1]} + (f32x2){bu[n][2 * jp], bu[n][2 * jp + 1]};
;                         g.x = fminf(g.x, 7.f); g.y = fminf(g.y, 7.f);
;                         uu.x = __builtin_amdgcn_fmed3f(uu.x, -6.f, 8.f); uu.y = __builtin_amdgcn_fmed3f(uu.y, -6.f, 8.f);
;                         f32x2 t = g * kk;
;                         t.x = __builtin_amdgcn_exp2f(t.x); t.y = __builtin_amdgcn_exp2f(t.y);
;                         t = t + one2;
;                         t.x = __builtin_amdgcn_rcpf(t.x); t.y = __builtin_amdgcn_rcpf(t.y);
;                         const f32x2 o = uu * (g * t);
;                         wv[n * 2 + jp] = cvt_pk_bf16(o.x, o.y); }
;                 u32x4 w; w.x = wv[0]; w.y = wv[1]; w.z = wv[2]; w.w = wv[3];
;                 *(u32x4*)(act + (size_t)(ai * HALF + m * 16) * 1024) = w; }
	v_pk_mul_f32 v[106:107], v[106:107], v[116:117]
	v_pk_add_f32 v[94:95], v[94:95], v[110:111]
	v_pk_mul_f32 v[102:103], v[102:103], v[106:107]
	v_pk_add_f32 v[106:107], v[118:119], 1.0 op_sel_hi:[1,0]
	v_cvt_pk_bf16_f32 v116, v102, v103
	v_med3_f32 v102, v104, s51, v163
	v_rcp_f32_e32 v106, v106
	v_rcp_f32_e32 v107, v107
	v_med3_f32 v103, v105, s51, v163
	v_min_f32_e32 v94, 0x40e00000, v94
	v_min_f32_e32 v95, 0x40e00000, v95
	v_pk_mul_f32 v[104:105], v[108:109], v[106:107]
	v_pk_add_f32 v[96:97], v[96:97], v[112:113]
	v_pk_mul_f32 v[102:103], v[102:103], v[104:105]
	v_min_f32_e32 v96, 0x40e00000, v96
	v_cvt_pk_bf16_f32 v117, v102, v103
	v_add_co_u32_e32 v102, vcc, s46, v146
	v_min_f32_e32 v97, 0x40e00000, v97
	s_nop 0
	v_addc_co_u32_e32 v103, vcc, 0, v147, vcc
	global_store_dwordx4 v[102:103], v[114:117], off
	v_pk_mul_f32 v[102:103], v[94:95], s[20:21] op_sel_hi:[1,0]
	v_pk_mul_f32 v[104:105], v[96:97], s[20:21] op_sel_hi:[1,0]
	v_exp_f32_e32 v102, v102
	v_exp_f32_e32 v103, v103
	v_exp_f32_e32 v104, v104
	v_exp_f32_e32 v105, v105
	v_pk_add_f32 v[90:91], v[90:91], v[132:133]
	v_pk_add_f32 v[102:103], v[102:103], 1.0 op_sel_hi:[1,0]
	v_med3_f32 v90, v90, s51, v163
	v_rcp_f32_e32 v102, v102
	v_rcp_f32_e32 v103, v103
	v_med3_f32 v91, v91, s51, v163
	v_pk_add_f32 v[92:93], v[92:93], v[130:131]
	v_pk_add_f32 v[86:87], v[86:87], v[98:99]
	v_pk_mul_f32 v[94:95], v[94:95], v[102:103]
	v_med3_f32 v92, v92, s51, v163
	v_pk_mul_f32 v[90:91], v[90:91], v[94:95]
	v_pk_add_f32 v[94:95], v[104:105], 1.0 op_sel_hi:[1,0]
	v_med3_f32 v93, v93, s51, v163
	v_rcp_f32_e32 v94, v94
	v_rcp_f32_e32 v95, v95
	v_min_f32_e32 v86, 0x40e00000, v86
	v_min_f32_e32 v87, 0x40e00000, v87
	v_cvt_pk_bf16_f32 v90, v90, v91
	v_pk_mul_f32 v[94:95], v[96:97], v[94:95]
	v_pk_add_f32 v[88:89], v[88:89], v[100:101]
	v_pk_mul_f32 v[92:93], v[92:93], v[94:95]
	v_min_f32_e32 v88, 0x40e00000, v88
	v_cvt_pk_bf16_f32 v91, v92, v93
	v_pk_mul_f32 v[92:93], v[86:87], s[20:21] op_sel_hi:[1,0]
	v_min_f32_e32 v89, 0x40e00000, v89
	v_exp_f32_e32 v92, v92
	v_exp_f32_e32 v93, v93
	v_pk_mul_f32 v[94:95], v[88:89], s[20:21] op_sel_hi:[1,0]
	v_pk_add_f32 v[82:83], v[82:83], v[150:151]
	v_exp_f32_e32 v94, v94
	v_pk_add_f32 v[92:93], v[92:93], 1.0 op_sel_hi:[1,0]
	v_exp_f32_e32 v95, v95
	v_rcp_f32_e32 v92, v92
	v_rcp_f32_e32 v93, v93
	v_med3_f32 v82, v82, s51, v163
	v_med3_f32 v83, v83, s51, v163
	v_pk_add_f32 v[84:85], v[84:85], v[148:149]
	v_pk_mul_f32 v[86:87], v[86:87], v[92:93]
	v_pk_add_f32 v[78:79], v[78:79], v[110:111]
	v_pk_mul_f32 v[82:83], v[82:83], v[86:87]
	v_pk_add_f32 v[86:87], v[94:95], 1.0 op_sel_hi:[1,0]
	v_cvt_pk_bf16_f32 v92, v82, v83
	v_med3_f32 v82, v84, s51, v163
	v_rcp_f32_e32 v86, v86
	v_rcp_f32_e32 v87, v87
	v_med3_f32 v83, v85, s51, v163
	v_min_f32_e32 v78, 0x40e00000, v78
	v_min_f32_e32 v79, 0x40e00000, v79
	v_pk_mul_f32 v[84:85], v[88:89], v[86:87]
	v_pk_add_f32 v[80:81], v[80:81], v[112:113]
	v_pk_mul_f32 v[82:83], v[82:83], v[84:85]
	v_min_f32_e32 v80, 0x40e00000, v80
	v_cvt_pk_bf16_f32 v93, v82, v83
	v_add_co_u32_e32 v82, vcc, s41, v146
	v_min_f32_e32 v81, 0x40e00000, v81
	s_nop 0
	v_addc_co_u32_e32 v83, vcc, 0, v147, vcc
	global_store_dwordx4 v[82:83], v[90:93], off
	v_pk_mul_f32 v[82:83], v[78:79], s[20:21] op_sel_hi:[1,0]
	v_pk_mul_f32 v[84:85], v[80:81], s[20:21] op_sel_hi:[1,0]
	v_exp_f32_e32 v82, v82
	v_exp_f32_e32 v83, v83
	v_exp_f32_e32 v84, v84
	v_exp_f32_e32 v85, v85
	v_pk_add_f32 v[74:75], v[74:75], v[132:133]
	v_pk_add_f32 v[82:83], v[82:83], 1.0 op_sel_hi:[1,0]
	v_med3_f32 v74, v74, s51, v163
	v_rcp_f32_e32 v82, v82
	v_rcp_f32_e32 v83, v83
	v_med3_f32 v75, v75, s51, v163
	v_pk_add_f32 v[76:77], v[76:77], v[130:131]
	v_pk_add_f32 v[70:71], v[70:71], v[98:99]
	v_pk_mul_f32 v[78:79], v[78:79], v[82:83]
	v_med3_f32 v76, v76, s51, v163
	v_pk_mul_f32 v[74:75], v[74:75], v[78:79]
	v_pk_add_f32 v[78:79], v[84:85], 1.0 op_sel_hi:[1,0]
	v_med3_f32 v77, v77, s51, v163
	v_rcp_f32_e32 v78, v78
	v_rcp_f32_e32 v79, v79
	v_min_f32_e32 v70, 0x40e00000, v70
	v_min_f32_e32 v71, 0x40e00000, v71
	v_cvt_pk_bf16_f32 v74, v74, v75
	v_pk_mul_f32 v[78:79], v[80:81], v[78:79]
	v_pk_add_f32 v[72:73], v[72:73], v[100:101]
	v_pk_mul_f32 v[76:77], v[76:77], v[78:79]
	v_min_f32_e32 v72, 0x40e00000, v72
	v_cvt_pk_bf16_f32 v75, v76, v77
	v_pk_mul_f32 v[76:77], v[70:71], s[20:21] op_sel_hi:[1,0]
	v_min_f32_e32 v73, 0x40e00000, v73
	v_exp_f32_e32 v76, v76
	v_exp_f32_e32 v77, v77
	v_pk_mul_f32 v[78:79], v[72:73], s[20:21] op_sel_hi:[1,0]
	v_pk_add_f32 v[66:67], v[66:67], v[150:151]
	v_exp_f32_e32 v78, v78
	v_pk_add_f32 v[76:77], v[76:77], 1.0 op_sel_hi:[1,0]
	v_exp_f32_e32 v79, v79
	v_rcp_f32_e32 v76, v76
	v_rcp_f32_e32 v77, v77
	v_med3_f32 v66, v66, s51, v163
	v_med3_f32 v67, v67, s51, v163
	v_pk_add_f32 v[68:69], v[68:69], v[148:149]
	v_pk_mul_f32 v[70:71], v[70:71], v[76:77]
	v_pk_add_f32 v[62:63], v[62:63], v[110:111]
	v_pk_mul_f32 v[66:67], v[66:67], v[70:71]
	v_pk_add_f32 v[70:71], v[78:79], 1.0 op_sel_hi:[1,0]
	v_cvt_pk_bf16_f32 v76, v66, v67
	v_med3_f32 v66, v68, s51, v163
	v_rcp_f32_e32 v70, v70
	v_rcp_f32_e32 v71, v71
	v_med3_f32 v67, v69, s51, v163
	v_min_f32_e32 v62, 0x40e00000, v62
	v_min_f32_e32 v63, 0x40e00000, v63
	v_pk_mul_f32 v[68:69], v[72:73], v[70:71]
	v_pk_add_f32 v[64:65], v[64:65], v[112:113]
	v_pk_mul_f32 v[66:67], v[66:67], v[68:69]
	v_min_f32_e32 v64, 0x40e00000, v64
	v_cvt_pk_bf16_f32 v77, v66, v67
	v_add_co_u32_e32 v66, vcc, s45, v146
	v_min_f32_e32 v65, 0x40e00000, v65
	s_nop 0
	v_addc_co_u32_e32 v67, vcc, 0, v147, vcc
	global_store_dwordx4 v[66:67], v[74:77], off
	v_pk_mul_f32 v[66:67], v[62:63], s[20:21] op_sel_hi:[1,0]
	v_pk_mul_f32 v[68:69], v[64:65], s[20:21] op_sel_hi:[1,0]
; __device__ __forceinline__ unsigned cvt_pk_bf16(float lo, float hi) { unsigned r; asm volatile("v_cvt_pk_bf16_f32 %0, %1, %2" : "=v"(r) : "v"(lo), "v"(hi)); return r; }
;     __device__ __forceinline__ void operator()(const f32x4 (&acc)[2][2][4][2], const Unit& u, int wr, int wc, int fr, int fq) const {
;     ...
; #pragma unroll
;         for (int ai = 0; ai < 2; ++ai)
; #pragma unroll
;             for (int m = 0; m < 4; ++m) { unsigned wv[4];
; #pragma unroll
;                 for (int n = 0; n < 2; ++n)
; #pragma unroll
;                     for (int jp = 0; jp < 2; ++jp) {
;                         f32x2 g = (f32x2){acc[ai][0][m][n][2 * jp], acc[ai][0][m][n][2 * jp + 1]} + (f32x2){bg[n][2 * jp], bg[n][2 * jp + 1]};
;                         f32x2 uu = (f32x2){acc[ai][1][m][n][2 * jp], acc[ai][1][m][n][2 * jp + 1]} + (f32x2){bu[n][2 * jp], bu[n][2 * jp + 1]};
;                         g.x = fminf(g.x, 7.f); g.y = fminf(g.y, 7.f);
;                         uu.x = __builtin_amdgcn_fmed3f(uu.x, -6.f, 8.f); uu.y = __builtin_amdgcn_fmed3f(uu.y, -6.f, 8.f);
;                         f32x2 t = g * kk;
;                         t.x = __builtin_amdgcn_exp2f(t.x); t.y = __builtin_amdgcn_exp2f(t.y);
;                         t = t + one2;
;                         t.x = __builtin_amdgcn_rcpf(t.x); t.y = __builtin_amdgcn_rcpf(t.y);
;                         const f32x2 o = uu * (g * t);
;                         wv[n * 2 + jp] = cvt_pk_bf16(o.x, o.y); }
;                 u32x4 w; w.x = wv[0]; w.y = wv[1]; w.z = wv[2]; w.w = wv[3];
;                 *(u32x4*)(act + (size_t)(ai * HALF + m * 16) * 1024) = w; }
	v_exp_f32_e32 v66, v66
	v_exp_f32_e32 v67, v67
	v_exp_f32_e32 v68, v68
	v_exp_f32_e32 v69, v69
	v_pk_add_f32 v[58:59], v[58:59], v[132:133]
	v_pk_add_f32 v[66:67], v[66:67], 1.0 op_sel_hi:[1,0]
	v_med3_f32 v58, v58, s51, v163
	v_rcp_f32_e32 v66, v66
	v_rcp_f32_e32 v67, v67
	v_med3_f32 v59, v59, s51, v163
	v_pk_add_f32 v[60:61], v[60:61], v[130:131]
	v_pk_add_f32 v[54:55], v[54:55], v[98:99]
	v_pk_mul_f32 v[62:63], v[62:63], v[66:67]
	v_med3_f32 v60, v60, s51, v163
	v_pk_mul_f32 v[58:59], v[58:59], v[62:63]
	v_pk_add_f32 v[62:63], v[68:69], 1.0 op_sel_hi:[1,0]
	v_med3_f32 v61, v61, s51, v163
	v_rcp_f32_e32 v62, v62
	v_rcp_f32_e32 v63, v63
	v_min_f32_e32 v54, 0x40e00000, v54
	v_min_f32_e32 v55, 0x40e00000, v55
	v_cvt_pk_bf16_f32 v58, v58, v59
	v_pk_mul_f32 v[62:63], v[64:65], v[62:63]
	v_pk_add_f32 v[56:57], v[56:57], v[100:101]
	v_pk_mul_f32 v[60:61], v[60:61], v[62:63]
	v_min_f32_e32 v56, 0x40e00000, v56
	v_cvt_pk_bf16_f32 v59, v60, v61
	v_pk_mul_f32 v[60:61], v[54:55], s[20:21] op_sel_hi:[1,0]
	v_min_f32_e32 v57, 0x40e00000, v57
	v_exp_f32_e32 v60, v60
	v_exp_f32_e32 v61, v61
	v_pk_mul_f32 v[62:63], v[56:57], s[20:21] op_sel_hi:[1,0]
	v_pk_add_f32 v[50:51], v[50:51], v[150:151]
	v_exp_f32_e32 v62, v62
	v_pk_add_f32 v[60:61], v[60:61], 1.0 op_sel_hi:[1,0]
	v_exp_f32_e32 v63, v63
	v_rcp_f32_e32 v60, v60
	v_rcp_f32_e32 v61, v61
	v_med3_f32 v50, v50, s51, v163
	v_med3_f32 v51, v51, s51, v163
	v_pk_add_f32 v[52:53], v[52:53], v[148:149]
	v_pk_mul_f32 v[54:55], v[54:55], v[60:61]
	v_pk_add_f32 v[46:47], v[46:47], v[110:111]
	v_pk_mul_f32 v[50:51], v[50:51], v[54:55]
	v_pk_add_f32 v[54:55], v[62:63], 1.0 op_sel_hi:[1,0]
	v_cvt_pk_bf16_f32 v60, v50, v51
	v_med3_f32 v50, v52, s51, v163
	v_rcp_f32_e32 v54, v54
	v_rcp_f32_e32 v55, v55
	v_med3_f32 v51, v53, s51, v163
	v_min_f32_e32 v46, 0x40e00000, v46
	v_min_f32_e32 v47, 0x40e00000, v47
	v_pk_mul_f32 v[52:53], v[56:57], v[54:55]
	v_pk_add_f32 v[48:49], v[48:49], v[112:113]
	v_pk_mul_f32 v[50:51], v[50:51], v[52:53]
	v_min_f32_e32 v48, 0x40e00000, v48
	v_cvt_pk_bf16_f32 v61, v50, v51
	v_add_co_u32_e32 v50, vcc, s49, v146
	v_min_f32_e32 v49, 0x40e00000, v49
	s_nop 0
	v_addc_co_u32_e32 v51, vcc, 0, v147, vcc
	global_store_dwordx4 v[50:51], v[58:61], off
	v_pk_mul_f32 v[50:51], v[46:47], s[20:21] op_sel_hi:[1,0]
	v_pk_mul_f32 v[52:53], v[48:49], s[20:21] op_sel_hi:[1,0]
	v_exp_f32_e32 v50, v50
	v_exp_f32_e32 v51, v51
	v_exp_f32_e32 v52, v52
	v_exp_f32_e32 v53, v53
	v_pk_add_f32 v[42:43], v[42:43], v[132:133]
	v_pk_add_f32 v[50:51], v[50:51], 1.0 op_sel_hi:[1,0]
	v_med3_f32 v42, v42, s51, v163
	v_rcp_f32_e32 v50, v50
	v_rcp_f32_e32 v51, v51
	v_med3_f32 v43, v43, s51, v163
	v_pk_add_f32 v[44:45], v[44:45], v[130:131]
	v_pk_add_f32 v[38:39], v[38:39], v[98:99]
	v_pk_mul_f32 v[46:47], v[46:47], v[50:51]
	v_med3_f32 v44, v44, s51, v163
	v_pk_mul_f32 v[42:43], v[42:43], v[46:47]
	v_pk_add_f32 v[46:47], v[52:53], 1.0 op_sel_hi:[1,0]
	v_med3_f32 v45, v45, s51, v163
	v_rcp_f32_e32 v46, v46
	v_rcp_f32_e32 v47, v47
	v_min_f32_e32 v38, 0x40e00000, v38
	v_min_f32_e32 v39, 0x40e00000, v39
	v_cvt_pk_bf16_f32 v42, v42, v43
	v_pk_mul_f32 v[46:47], v[48:49], v[46:47]
	v_pk_add_f32 v[40:41], v[40:41], v[100:101]
	v_pk_mul_f32 v[44:45], v[44:45], v[46:47]
	v_min_f32_e32 v40, 0x40e00000, v40
	v_cvt_pk_bf16_f32 v43, v44, v45
	v_pk_mul_f32 v[44:45], v[38:39], s[20:21] op_sel_hi:[1,0]
	v_min_f32_e32 v41, 0x40e00000, v41
	v_exp_f32_e32 v44, v44
	v_exp_f32_e32 v45, v45
	v_pk_mul_f32 v[46:47], v[40:41], s[20:21] op_sel_hi:[1,0]
	v_pk_add_f32 v[34:35], v[34:35], v[150:151]
	v_exp_f32_e32 v46, v46
	v_pk_add_f32 v[44:45], v[44:45], 1.0 op_sel_hi:[1,0]
	v_exp_f32_e32 v47, v47
	v_rcp_f32_e32 v44, v44
	v_rcp_f32_e32 v45, v45
	v_med3_f32 v34, v34, s51, v163
	v_med3_f32 v35, v35, s51, v163
	v_pk_add_f32 v[36:37], v[36:37], v[148:149]
	v_pk_mul_f32 v[38:39], v[38:39], v[44:45]
	v_pk_add_f32 v[30:31], v[30:31], v[110:111]
	v_pk_mul_f32 v[34:35], v[34:35], v[38:39]
	v_pk_add_f32 v[38:39], v[46:47], 1.0 op_sel_hi:[1,0]
	v_cvt_pk_bf16_f32 v44, v34, v35
	v_med3_f32 v34, v36, s51, v163
	v_rcp_f32_e32 v38, v38
	v_rcp_f32_e32 v39, v39
	v_med3_f32 v35, v37, s51, v163
	v_min_f32_e32 v30, 0x40e00000, v30
	v_min_f32_e32 v31, 0x40e00000, v31
	v_pk_mul_f32 v[36:37], v[40:41], v[38:39]
	v_pk_add_f32 v[32:33], v[32:33], v[112:113]
	v_pk_mul_f32 v[34:35], v[34:35], v[36:37]
	v_min_f32_e32 v32, 0x40e00000, v32
	v_cvt_pk_bf16_f32 v45, v34, v35
	v_add_co_u32_e32 v34, vcc, s52, v146
	v_min_f32_e32 v33, 0x40e00000, v33
	s_nop 0
	v_addc_co_u32_e32 v35, vcc, 0, v147, vcc
	global_store_dwordx4 v[34:35], v[42:45], off
; __device__ __forceinline__ unsigned cvt_pk_bf16(float lo, float hi) { unsigned r; asm volatile("v_cvt_pk_bf16_f32 %0, %1, %2" : "=v"(r) : "v"(lo), "v"(hi)); return r; }
; template <class Epi, class Sched, bool GATHER, bool ALIGN_EPI, bool PFB = false>
; __device__ __forceinline__ void gemm_phase(LAS unsigned char* lds, const int lda, const int K, const Sched& S, const Epi& E) {
;     ...
;         if (!has_next) break;
; #pragma unroll
;         for (int a = 0; a < 2; ++a)
; #pragma unroll
;             for (int b = 0; b < 2; ++b)
; #pragma unroll
;                 for (int m = 0; m < 4; ++m)
; #pragma unroll
;                     for (int n = 0; n < 2; ++n) acc[a][b][m][n] = (f32x4){0.f, 0.f, 0.f, 0.f};
;         cur = nxt; cA = nA; cB = nB; ++ui;
;         if (GATHER) {
; #pragma unroll
;             for (int i = 0; i < 2; ++i) { vA0[i] = nA0[i]; vA1[i] = nA1[i]; }
;         }
;         if constexpr (ALIGN_EPI) { if (wr == 1) G8_BAR; }
;     }
;     __device__ __forceinline__ void operator()(const f32x4 (&acc)[2][2][4][2], const Unit& u, int wr, int wc, int fr, int fq) const {
;     ...
; #pragma unroll
;         for (int ai = 0; ai < 2; ++ai)
; #pragma unroll
;             for (int m = 0; m < 4; ++m) { unsigned wv[4];
; #pragma unroll
;                 for (int n = 0; n < 2; ++n)
; #pragma unroll
;                     for (int jp = 0; jp < 2; ++jp) {
;                         f32x2 g = (f32x2){acc[ai][0][m][n][2 * jp], acc[ai][0][m][n][2 * jp + 1]} + (f32x2){bg[n][2 * jp], bg[n][2 * jp + 1]};
;                         f32x2 uu = (f32x2){acc[ai][1][m][n][2 * jp], acc[ai][1][m][n][2 * jp + 1]} + (f32x2){bu[n][2 * jp], bu[n][2 * jp + 1]};
;                         g.x = fminf(g.x, 7.f); g.y = fminf(g.y, 7.f);
;                         uu.x = __builtin_amdgcn_fmed3f(uu.x, -6.f, 8.f); uu.y = __builtin_amdgcn_fmed3f(uu.y, -6.f, 8.f);
;                         f32x2 t = g * kk;
;                         t.x = __builtin_amdgcn_exp2f(t.x); t.y = __builtin_amdgcn_exp2f(t.y);
;                         t = t + one2;
;                         t.x = __builtin_amdgcn_rcpf(t.x); t.y = __builtin_amdgcn_rcpf(t.y);
;                         const f32x2 o = uu * (g * t);
;                         wv[n * 2 + jp] = cvt_pk_bf16(o.x, o.y); }
;                 u32x4 w; w.x = wv[0]; w.y = wv[1]; w.z = wv[2]; w.w = wv[3];
;                 *(u32x4*)(act + (size_t)(ai * HALF + m * 16) * 1024) = w; }
	v_pk_mul_f32 v[34:35], v[30:31], s[20:21] op_sel_hi:[1,0]
	v_pk_mul_f32 v[36:37], v[32:33], s[20:21] op_sel_hi:[1,0]
	v_exp_f32_e32 v34, v34
	v_exp_f32_e32 v35, v35
	v_exp_f32_e32 v36, v36
	v_exp_f32_e32 v37, v37
	v_pk_add_f32 v[26:27], v[26:27], v[132:133]
	v_pk_add_f32 v[34:35], v[34:35], 1.0 op_sel_hi:[1,0]
	v_med3_f32 v26, v26, s51, v163
	v_rcp_f32_e32 v34, v34
	v_rcp_f32_e32 v35, v35
	v_med3_f32 v27, v27, s51, v163
	v_pk_add_f32 v[28:29], v[28:29], v[130:131]
	v_pk_add_f32 v[22:23], v[22:23], v[98:99]
	v_pk_mul_f32 v[30:31], v[30:31], v[34:35]
	v_med3_f32 v28, v28, s51, v163
	v_pk_mul_f32 v[26:27], v[26:27], v[30:31]
	v_pk_add_f32 v[30:31], v[36:37], 1.0 op_sel_hi:[1,0]
	v_med3_f32 v29, v29, s51, v163
	v_rcp_f32_e32 v30, v30
	v_rcp_f32_e32 v31, v31
	v_min_f32_e32 v22, 0x40e00000, v22
	v_min_f32_e32 v23, 0x40e00000, v23
	v_cvt_pk_bf16_f32 v26, v26, v27
	v_pk_mul_f32 v[30:31], v[32:33], v[30:31]
	v_pk_add_f32 v[24:25], v[24:25], v[100:101]
	v_pk_mul_f32 v[28:29], v[28:29], v[30:31]
	v_min_f32_e32 v24, 0x40e00000, v24
	v_cvt_pk_bf16_f32 v27, v28, v29
	v_pk_mul_f32 v[28:29], v[22:23], s[20:21] op_sel_hi:[1,0]
	v_min_f32_e32 v25, 0x40e00000, v25
	v_exp_f32_e32 v28, v28
	v_exp_f32_e32 v29, v29
	v_pk_mul_f32 v[30:31], v[24:25], s[20:21] op_sel_hi:[1,0]
	v_pk_add_f32 v[18:19], v[18:19], v[150:151]
	v_exp_f32_e32 v30, v30
	v_pk_add_f32 v[28:29], v[28:29], 1.0 op_sel_hi:[1,0]
	v_exp_f32_e32 v31, v31
	v_rcp_f32_e32 v28, v28
	v_rcp_f32_e32 v29, v29
	v_med3_f32 v18, v18, s51, v163
	v_med3_f32 v19, v19, s51, v163
	v_pk_add_f32 v[20:21], v[20:21], v[148:149]
	v_pk_mul_f32 v[22:23], v[22:23], v[28:29]
	v_pk_add_f32 v[14:15], v[14:15], v[110:111]
	v_pk_mul_f32 v[18:19], v[18:19], v[22:23]
	v_pk_add_f32 v[22:23], v[30:31], 1.0 op_sel_hi:[1,0]
	v_cvt_pk_bf16_f32 v28, v18, v19
	v_med3_f32 v18, v20, s51, v163
	v_rcp_f32_e32 v22, v22
	v_rcp_f32_e32 v23, v23
	v_med3_f32 v19, v21, s51, v163
	v_min_f32_e32 v14, 0x40e00000, v14
	v_min_f32_e32 v15, 0x40e00000, v15
	v_pk_mul_f32 v[20:21], v[24:25], v[22:23]
	v_pk_add_f32 v[16:17], v[16:17], v[112:113]
	v_pk_mul_f32 v[18:19], v[18:19], v[20:21]
	v_min_f32_e32 v16, 0x40e00000, v16
	v_cvt_pk_bf16_f32 v29, v18, v19
	v_add_co_u32_e32 v18, vcc, s53, v146
	v_min_f32_e32 v17, 0x40e00000, v17
	s_nop 0
	v_addc_co_u32_e32 v19, vcc, 0, v147, vcc
	global_store_dwordx4 v[18:19], v[26:29], off
	v_pk_mul_f32 v[18:19], v[14:15], s[20:21] op_sel_hi:[1,0]
	v_pk_mul_f32 v[20:21], v[16:17], s[20:21] op_sel_hi:[1,0]
	v_exp_f32_e32 v18, v18
	v_exp_f32_e32 v19, v19
	v_exp_f32_e32 v20, v20
	v_exp_f32_e32 v21, v21
	v_pk_add_f32 v[10:11], v[10:11], v[132:133]
	v_pk_add_f32 v[18:19], v[18:19], 1.0 op_sel_hi:[1,0]
	v_med3_f32 v10, v10, s51, v163
	v_rcp_f32_e32 v18, v18
	v_rcp_f32_e32 v19, v19
	v_med3_f32 v11, v11, s51, v163
	v_pk_add_f32 v[12:13], v[12:13], v[130:131]
	v_pk_add_f32 v[6:7], v[6:7], v[98:99]
	v_pk_mul_f32 v[14:15], v[14:15], v[18:19]
	v_med3_f32 v12, v12, s51, v163
	v_pk_mul_f32 v[10:11], v[10:11], v[14:15]
	v_pk_add_f32 v[14:15], v[20:21], 1.0 op_sel_hi:[1,0]
	v_med3_f32 v13, v13, s51, v163
	v_rcp_f32_e32 v14, v14
	v_rcp_f32_e32 v15, v15
	v_min_f32_e32 v6, 0x40e00000, v6
	v_min_f32_e32 v7, 0x40e00000, v7
	v_cvt_pk_bf16_f32 v10, v10, v11
	v_pk_mul_f32 v[14:15], v[16:17], v[14:15]
	v_pk_add_f32 v[8:9], v[8:9], v[100:101]
	v_pk_mul_f32 v[12:13], v[12:13], v[14:15]
	v_min_f32_e32 v8, 0x40e00000, v8
	v_cvt_pk_bf16_f32 v11, v12, v13
	v_pk_mul_f32 v[12:13], v[6:7], s[20:21] op_sel_hi:[1,0]
	v_min_f32_e32 v9, 0x40e00000, v9
	v_exp_f32_e32 v12, v12
	v_exp_f32_e32 v13, v13
	v_pk_mul_f32 v[14:15], v[8:9], s[20:21] op_sel_hi:[1,0]
	v_pk_add_f32 v[2:3], v[2:3], v[150:151]
	v_exp_f32_e32 v14, v14
	v_pk_add_f32 v[12:13], v[12:13], 1.0 op_sel_hi:[1,0]
	v_exp_f32_e32 v15, v15
	v_rcp_f32_e32 v12, v12
	v_rcp_f32_e32 v13, v13
	v_med3_f32 v2, v2, s51, v163
	v_med3_f32 v3, v3, s51, v163
	v_pk_add_f32 v[4:5], v[4:5], v[148:149]
	v_pk_mul_f32 v[6:7], v[6:7], v[12:13]
	s_nop 0
	v_pk_mul_f32 v[2:3], v[2:3], v[6:7]
	v_pk_add_f32 v[6:7], v[14:15], 1.0 op_sel_hi:[1,0]
	v_cvt_pk_bf16_f32 v12, v2, v3
	v_med3_f32 v2, v4, s51, v163
	v_rcp_f32_e32 v6, v6
	v_rcp_f32_e32 v7, v7
	v_med3_f32 v3, v5, s51, v163
	v_pk_mul_f32 v[4:5], v[8:9], v[6:7]
	s_nop 0
	v_pk_mul_f32 v[2:3], v[2:3], v[4:5]
	s_nop 0
	v_cvt_pk_bf16_f32 v13, v2, v3
	v_add_co_u32_e32 v2, vcc, 0x58000, v146
	s_nop 1
	v_addc_co_u32_e32 v3, vcc, 0, v147, vcc
	s_and_b64 vcc, exec, s[4:5]
	global_store_dwordx4 v[2:3], v[10:13], off
	s_cbranch_vccnz .LBB0_2356
	s_andn2_b64 vcc, exec, s[6:7]
	s_cbranch_vccnz .LBB0_2355
	s_barrier
	s_branch .LBB0_2355
